# speedup vs baseline: 1.0438x; 1.0037x over previous
_Z6gemm_kILi1ELi0ELi2ELi3EEvPKvS1_S1_S1_PvS2_PKfiiiiiilllf:
	s_load_dwordx2 s[12:13], s[0:1], 0x48
	s_load_dwordx4 s[4:7], s[0:1], 0x38
	s_load_dwordx2 s[26:27], s[0:1], 0x0
	s_load_dwordx2 s[28:29], s[0:1], 0x10
	s_load_dword s3, s[0:1], 0x70
	s_waitcnt lgkmcnt(0)
	s_mul_i32 s14, s13, s12
	s_abs_i32 s8, s14
	v_cvt_f32_u32_e32 v1, s8
	s_and_b32 s9, s2, 7
	s_ashr_i32 s3, s3, 3
	s_sub_i32 s10, 0, s8
	v_rcp_iflag_f32_e32 v1, v1
	s_mul_i32 s3, s3, s9
	s_ashr_i32 s2, s2, 3
	s_add_i32 s3, s3, s2
	v_mul_f32_e32 v1, 0x4f7ffffe, v1
	v_cvt_u32_f32_e32 v1, v1
	s_abs_i32 s9, s3
	s_xor_b32 s2, s3, s14
	s_ashr_i32 s2, s2, 31
	v_readfirstlane_b32 s11, v1
	s_mul_i32 s10, s10, s11
	s_mul_hi_u32 s10, s11, s10
	s_add_i32 s11, s11, s10
	s_mul_hi_u32 s10, s9, s11
	s_mul_i32 s11, s10, s8
	s_sub_i32 s9, s9, s11
	s_add_i32 s11, s10, 1
	s_sub_i32 s12, s9, s8
	s_cmp_ge_u32 s9, s8
	s_cselect_b32 s10, s11, s10
	s_cselect_b32 s9, s12, s9
	s_add_i32 s11, s10, 1
	s_cmp_ge_u32 s9, s8
	s_cselect_b32 s12, s11, s10
	s_abs_i32 s15, s13
	v_cvt_f32_u32_e32 v1, s15
	s_xor_b32 s12, s12, s2
	s_sub_i32 s12, s12, s2
	s_sub_i32 s16, 0, s15
	v_rcp_iflag_f32_e32 v1, v1
	s_mul_i32 s2, s12, s14
	s_sub_i32 s2, s3, s2
	s_abs_i32 s14, s2
	v_mul_f32_e32 v1, 0x4f7ffffe, v1
	v_cvt_u32_f32_e32 v1, v1
	s_xor_b32 s3, s2, s13
	s_ashr_i32 s3, s3, 31
	s_load_dwordx4 s[8:11], s[0:1], 0x50
	v_readfirstlane_b32 s17, v1
	s_mul_i32 s16, s16, s17
	s_mul_hi_u32 s16, s17, s16
	s_add_i32 s17, s17, s16
	s_mul_hi_u32 s16, s14, s17
	s_mul_i32 s17, s16, s15
	s_sub_i32 s14, s14, s17
	s_add_i32 s17, s16, 1
	s_sub_i32 s18, s14, s15
	s_cmp_ge_u32 s14, s15
	s_cselect_b32 s16, s17, s16
	s_cselect_b32 s14, s18, s14
	s_add_i32 s17, s16, 1
	s_cmp_ge_u32 s14, s15
	s_cselect_b32 s14, s17, s16
	s_xor_b32 s14, s14, s3
	s_sub_i32 s3, s14, s3
	s_mul_i32 s13, s3, s13
	s_sub_i32 s14, s2, s13
	s_ashr_i32 s13, s12, 31
	s_lshl_b32 s33, s3, 8
	s_waitcnt lgkmcnt(0)
	s_mul_i32 s2, s8, s13
	s_mul_hi_u32 s3, s8, s12
	s_add_i32 s2, s3, s2
	s_mul_i32 s3, s9, s12
	s_lshl_b32 s16, s14, 8
	s_add_i32 s3, s2, s3
	s_mul_i32 s2, s8, s12
	s_ashr_i32 s19, s4, 31
	s_mul_i32 s9, s33, s4
	s_mul_hi_i32 s8, s33, s4
	s_add_u32 s2, s9, s2
	s_addc_u32 s3, s8, s3
	s_lshl_b64 s[30:31], s[2:3], 1
	s_mul_i32 s2, s10, s13
	s_mul_hi_u32 s3, s10, s12
	s_add_i32 s2, s3, s2
	s_mul_i32 s3, s11, s12
	s_add_i32 s3, s2, s3
	s_mul_i32 s2, s10, s12
	s_ashr_i32 s35, s5, 31
	s_mul_i32 s9, s16, s5
	s_mul_hi_i32 s8, s16, s5
	s_add_u32 s2, s9, s2
	s_addc_u32 s3, s8, s3
	s_lshl_b64 s[36:37], s[2:3], 2
	s_add_u32 s2, s26, s30
	s_addc_u32 s3, s27, s31
	v_lshrrev_b32_e32 v201, 2, v0
	s_add_u32 s8, s28, s36
	s_mov_b32 s18, s4
	v_mul_lo_u32 v1, s4, v201
	v_lshlrev_b32_e32 v26, 3, v0
	s_addc_u32 s9, s29, s37
	s_ashr_i32 s4, s7, 31
	v_and_b32_e32 v2, 24, v26
	s_lshr_b32 s4, s4, 27
	v_add_lshl_u32 v144, v1, v2, 1
	s_add_i32 s4, s7, s4
	v_lshrrev_b32_e32 v1, 3, v0
	v_lshlrev_b32_e32 v10, 2, v0
	s_ashr_i32 s15, s4, 5
	s_lshl_b64 s[20:21], s[18:19], 8
	v_mul_lo_u32 v1, s5, v1
	v_and_b32_e32 v10, 28, v10
	s_add_u32 s10, s2, s20
	v_add_lshl_u32 v194, v1, v10, 2
	global_load_dwordx4 v[2:5], v144, s[2:3]
	s_addc_u32 s11, s3, s21
	global_load_dwordx4 v[10:13], v194, s[8:9]
	global_load_dwordx4 v[6:9], v144, s[10:11]
	s_mov_b32 s34, s5
	s_lshl_b64 s[22:23], s[34:35], 8
	s_add_u32 s4, s8, s22
	s_addc_u32 s5, s9, s23
	global_load_dwordx4 v[14:17], v194, s[4:5]
	s_add_u32 s4, s4, s22
	s_addc_u32 s5, s5, s23
	global_load_dwordx4 v[18:21], v194, s[4:5]
	s_add_u32 s4, s4, s22
	s_addc_u32 s5, s5, s23
	s_lshl_b64 s[24:25], s[34:35], 9
	s_sub_u32 s17, 0, s24
	s_subb_u32 s35, 0, s25
	global_load_dwordx4 v[22:25], v194, s[4:5]
	global_load_dwordx4 v[146:149], v144, s[2:3] offset:64
	global_load_dwordx4 v[150:153], v194, s[8:9] offset:128
	s_add_u32 s4, s4, s17
	s_addc_u32 s5, s5, s35
	s_add_u32 s38, s4, s22
	s_addc_u32 s39, s5, s23
	global_load_dwordx4 v[154:157], v194, s[4:5] offset:128
	global_load_dwordx4 v[158:161], v194, s[38:39] offset:128
	s_add_u32 s4, s38, s22
	s_addc_u32 s5, s39, s23
	global_load_dwordx4 v[166:169], v144, s[2:3] offset:128
	global_load_dwordx4 v[162:165], v144, s[10:11] offset:64
	global_load_dwordx4 v[170:173], v144, s[10:11] offset:128
	global_load_dwordx4 v[174:177], v194, s[8:9] offset:256
	s_add_u32 s2, s4, s17
	s_addc_u32 s3, s5, s35
	global_load_dwordx4 v[178:181], v194, s[4:5] offset:128
	global_load_dwordx4 v[182:185], v194, s[2:3] offset:256
	s_add_u32 s2, s2, s22
	s_addc_u32 s3, s3, s23
	s_add_u32 s4, s2, s22
	s_addc_u32 s5, s3, s23
	global_load_dwordx4 v[186:189], v194, s[2:3] offset:256
	global_load_dwordx4 v[190:193], v194, s[4:5] offset:256
	v_lshlrev_b32_e32 v27, 4, v0
	v_and_b32_e32 v28, 0x1fc0, v27
	v_xor_b32_e32 v27, v27, v0
	v_and_or_b32 v199, v27, 48, v28
	v_lshrrev_b32_e32 v196, 5, v0
	s_load_dwordx2 s[18:19], s[0:1], 0x60
	s_movk_i32 s4, 0xff
	s_cmp_gt_i32 s7, 31
	v_cmp_lt_u32_e32 vcc, s4, v0
	s_cselect_b64 s[4:5], -1, 0
	v_mov_b32_e32 v145, 0
	s_movk_i32 s2, 0x100
	s_waitcnt vmcnt(17)
	ds_write_b128 v199, v[2:5]
	s_waitcnt vmcnt(15)
	ds_write_b128 v199, v[6:9] offset:8192
	v_lshrrev_b32_e32 v2, 1, v0
	v_cvt_f16_f32_e32 v4, v10
	v_cvt_f16_f32_e32 v5, v11
	v_xor_b32_e32 v2, v2, v196
	v_lshlrev_b32_e32 v2, 4, v2
	v_and_b32_e32 v3, 0xfc8, v26
	v_and_or_b32 v200, v2, 48, v3
	v_cvt_pk_f16_f32 v3, v12, v13
	v_cvt_f32_f16_e32 v6, v4
	v_cvt_f32_f16_e32 v7, v5
	v_cvt_f32_f16_e32 v4, v3
	v_cvt_f32_f16_sdwa v5, v3 dst_sel:DWORD dst_unused:UNUSED_PAD src0_sel:WORD_1
	s_waitcnt vmcnt(14)
	v_cvt_f16_f32_e32 v8, v14
	v_cvt_f16_f32_e32 v9, v15
	v_sub_f32_e32 v6, v10, v6
	v_sub_f32_e32 v7, v11, v7
	v_pk_add_f32 v[4:5], v[12:13], v[4:5] neg_lo:[0,1] neg_hi:[0,1]
	v_cvt_pk_f16_f32 v6, v6, v7
	v_cvt_pk_f16_f32 v7, v4, v5
	v_cvt_pk_f16_f32 v5, v16, v17
	v_cvt_pk_f16_f32 v2, v10, v11
	v_cvt_f32_f16_e32 v10, v8
	v_cvt_f32_f16_e32 v11, v9
	v_cvt_f32_f16_e32 v8, v5
	v_cvt_f32_f16_sdwa v9, v5 dst_sel:DWORD dst_unused:UNUSED_PAD src0_sel:WORD_1
	v_cvt_pk_f16_f32 v4, v14, v15
	v_sub_f32_e32 v10, v14, v10
	v_sub_f32_e32 v11, v15, v11
	v_pk_add_f32 v[8:9], v[16:17], v[8:9] neg_lo:[0,1] neg_hi:[0,1]
	v_cvt_pk_f16_f32 v10, v10, v11
	v_cvt_pk_f16_f32 v11, v8, v9
	ds_write2st64_b64 v200, v[2:3], v[4:5] offset0:64 offset1:72
	ds_write2st64_b64 v200, v[6:7], v[10:11] offset0:96 offset1:104
	s_waitcnt vmcnt(13)
	v_cvt_f16_f32_e32 v3, v18
	v_cvt_f16_f32_e32 v4, v19
	s_waitcnt vmcnt(12)
	v_cvt_f16_f32_e32 v8, v22
	v_cvt_f16_f32_e32 v9, v23
	v_cvt_f32_f16_e32 v6, v3
	v_cvt_pk_f16_f32 v3, v20, v21
	v_cvt_f32_f16_e32 v7, v4
	v_cvt_f32_f16_e32 v4, v3
	v_cvt_f32_f16_sdwa v5, v3 dst_sel:DWORD dst_unused:UNUSED_PAD src0_sel:WORD_1
	v_sub_f32_e32 v6, v18, v6
	v_sub_f32_e32 v7, v19, v7
	v_cvt_pk_f16_f32 v6, v6, v7
	v_pk_add_f32 v[4:5], v[20:21], v[4:5] neg_lo:[0,1] neg_hi:[0,1]
	v_cvt_f32_f16_e32 v10, v8
	v_cvt_pk_f16_f32 v7, v4, v5
	v_cvt_pk_f16_f32 v5, v24, v25
	v_cvt_f32_f16_e32 v11, v9
	v_cvt_f32_f16_e32 v8, v5
	v_cvt_f32_f16_sdwa v9, v5 dst_sel:DWORD dst_unused:UNUSED_PAD src0_sel:WORD_1
	v_cvt_pk_f16_f32 v2, v18, v19
	v_cvt_pk_f16_f32 v4, v22, v23
	v_sub_f32_e32 v10, v22, v10
	v_sub_f32_e32 v11, v23, v11
	v_pk_add_f32 v[8:9], v[24:25], v[8:9] neg_lo:[0,1] neg_hi:[0,1]
	v_cvt_pk_f16_f32 v10, v10, v11
	v_cvt_pk_f16_f32 v11, v8, v9
	ds_write2st64_b64 v200, v[2:3], v[4:5] offset0:80 offset1:88
	ds_write2st64_b64 v200, v[6:7], v[10:11] offset0:112 offset1:120
	v_cndmask_b32_e64 v2, 0, 1, s[4:5]
	v_and_b32_e32 v1, 63, v0
	v_lshrrev_b32_e32 v197, 8, v0
	v_bfe_u32 v198, v0, 6, 2
	v_mov_b32_e32 v195, v145
	v_or_b32_e32 v202, 0x2000, v200
	v_cmp_gt_u32_e64 s[2:3], s2, v0
	v_cmp_ne_u32_e64 s[4:5], 1, v2
	s_waitcnt lgkmcnt(0)
	s_barrier
	s_and_saveexec_b64 s[8:9], vcc
	s_xor_b64 s[8:9], exec, s[8:9]
	s_cbranch_execz .LBB3_11
	s_and_b64 vcc, exec, s[4:5]
	v_mov_b32_e32 v128, 0
	v_mov_b32_e32 v143, 0
	v_mov_b32_e32 v142, 0
	v_mov_b32_e32 v141, 0
	v_mov_b32_e32 v140, 0
	v_mov_b32_e32 v139, 0
	v_mov_b32_e32 v138, 0
	v_mov_b32_e32 v137, 0
	v_mov_b32_e32 v136, 0
	v_mov_b32_e32 v135, 0
	v_mov_b32_e32 v134, 0
	v_mov_b32_e32 v133, 0
	v_mov_b32_e32 v132, 0
	v_mov_b32_e32 v131, 0
	v_mov_b32_e32 v130, 0
	v_mov_b32_e32 v113, 0
	v_mov_b32_e32 v112, 0
	v_mov_b32_e32 v111, 0
	v_mov_b32_e32 v110, 0
	v_mov_b32_e32 v109, 0
	v_mov_b32_e32 v108, 0
	v_mov_b32_e32 v107, 0
	v_mov_b32_e32 v106, 0
	v_mov_b32_e32 v105, 0
	v_mov_b32_e32 v104, 0
	v_mov_b32_e32 v103, 0
	v_mov_b32_e32 v102, 0
	v_mov_b32_e32 v101, 0
	v_mov_b32_e32 v100, 0
	v_mov_b32_e32 v99, 0
	v_mov_b32_e32 v98, 0
	v_mov_b32_e32 v97, 0
	v_mov_b32_e32 v96, 0
	v_mov_b32_e32 v95, 0
	v_mov_b32_e32 v94, 0
	v_mov_b32_e32 v93, 0
	v_mov_b32_e32 v92, 0
	v_mov_b32_e32 v91, 0
	v_mov_b32_e32 v90, 0
	v_mov_b32_e32 v89, 0
	v_mov_b32_e32 v88, 0
	v_mov_b32_e32 v87, 0
	v_mov_b32_e32 v86, 0
	v_mov_b32_e32 v85, 0
	v_mov_b32_e32 v84, 0
	v_mov_b32_e32 v83, 0
	v_mov_b32_e32 v82, 0
	v_mov_b32_e32 v81, 0
	v_mov_b32_e32 v80, 0
	v_mov_b32_e32 v79, 0
	v_mov_b32_e32 v78, 0
	v_mov_b32_e32 v77, 0
	v_mov_b32_e32 v76, 0
	v_mov_b32_e32 v75, 0
	v_mov_b32_e32 v74, 0
	v_mov_b32_e32 v73, 0
	v_mov_b32_e32 v72, 0
	v_mov_b32_e32 v71, 0
	v_mov_b32_e32 v70, 0
	v_mov_b32_e32 v69, 0
	v_mov_b32_e32 v68, 0
	v_mov_b32_e32 v67, 0
	v_mov_b32_e32 v66, 0
	v_mov_b32_e32 v65, 0
	v_mov_b32_e32 v64, 0
	v_mov_b32_e32 v63, 0
	v_mov_b32_e32 v62, 0
	v_mov_b32_e32 v61, 0
	v_mov_b32_e32 v60, 0
	v_mov_b32_e32 v59, 0
	v_mov_b32_e32 v58, 0
	v_mov_b32_e32 v57, 0
	v_mov_b32_e32 v56, 0
	v_mov_b32_e32 v55, 0
	v_mov_b32_e32 v54, 0
	v_mov_b32_e32 v53, 0
	v_mov_b32_e32 v52, 0
	v_mov_b32_e32 v51, 0
	v_mov_b32_e32 v50, 0
	v_mov_b32_e32 v49, 0
	v_mov_b32_e32 v48, 0
	v_mov_b32_e32 v47, 0
	v_mov_b32_e32 v46, 0
	v_mov_b32_e32 v45, 0
	v_mov_b32_e32 v44, 0
	v_mov_b32_e32 v43, 0
	v_mov_b32_e32 v42, 0
	v_mov_b32_e32 v41, 0
	v_mov_b32_e32 v40, 0
	v_mov_b32_e32 v39, 0
	v_mov_b32_e32 v38, 0
	v_mov_b32_e32 v37, 0
	v_mov_b32_e32 v36, 0
	v_mov_b32_e32 v35, 0
	v_mov_b32_e32 v34, 0
	v_mov_b32_e32 v33, 0
	v_mov_b32_e32 v32, 0
	v_mov_b32_e32 v31, 0
	v_mov_b32_e32 v30, 0
	v_mov_b32_e32 v29, 0
	v_mov_b32_e32 v28, 0
	v_mov_b32_e32 v27, 0
	v_mov_b32_e32 v26, 0
	v_mov_b32_e32 v25, 0
	v_mov_b32_e32 v24, 0
	v_mov_b32_e32 v23, 0
	v_mov_b32_e32 v22, 0
	v_mov_b32_e32 v21, 0
	v_mov_b32_e32 v20, 0
	v_mov_b32_e32 v19, 0
	v_mov_b32_e32 v18, 0
	v_mov_b32_e32 v17, 0
	v_mov_b32_e32 v16, 0
	v_mov_b32_e32 v15, 0
	v_mov_b32_e32 v14, 0
	v_mov_b32_e32 v13, 0
	v_mov_b32_e32 v12, 0
	v_mov_b32_e32 v11, 0
	v_mov_b32_e32 v10, 0
	v_mov_b32_e32 v9, 0
	v_mov_b32_e32 v8, 0
	v_mov_b32_e32 v7, 0
	v_mov_b32_e32 v6, 0
	v_mov_b32_e32 v5, 0
	v_mov_b32_e32 v4, 0
	v_mov_b32_e32 v3, 0
	v_mov_b32_e32 v2, 0
	s_cbranch_vccnz .LBB3_10
	v_lshlrev_b32_e32 v5, 6, v0
	v_lshrrev_b32_e32 v2, 5, v1
	v_bfe_u32 v3, v0, 2, 2
	v_and_b32_e32 v5, 0x7c0, v5
	s_add_u32 s10, s28, s36
	v_bitop3_b32 v4, v2, v201, 3 bitop3:0x78
	v_lshl_or_b32 v6, v197, 13, v5
	v_lshl_or_b32 v5, v198, 12, v5
	v_bitop3_b32 v2, v2, v3, 2 bitop3:0x36
	s_addc_u32 s11, s29, s37
	v_lshlrev_b32_e32 v4, 4, v4
	v_or_b32_e32 v7, 0x800, v6
	v_or_b32_e32 v9, 0x1000, v6
	v_or_b32_e32 v11, 0x1800, v6
	v_or_b32_e32 v13, 0x800, v5
	v_lshlrev_b32_e32 v2, 4, v2
	s_add_u32 s38, s26, s30
	v_or_b32_e32 v118, v4, v6
	v_or_b32_e32 v8, v7, v4
	v_or_b32_e32 v10, v9, v4
	v_or_b32_e32 v12, v11, v4
	v_or_b32_e32 v119, v5, v4
	v_or_b32_e32 v120, v13, v4
	v_or_b32_e32 v121, v2, v6
	v_or_b32_e32 v4, v2, v7
	v_or_b32_e32 v6, v2, v9
	v_or_b32_e32 v7, v2, v11
	v_or_b32_e32 v122, v2, v5
	v_or_b32_e32 v123, v13, v2
	v_lshl_add_u64 v[2:3], s[10:11], 0, v[194:195]
	s_mov_b64 s[10:11], 0x200
	s_addc_u32 s39, s27, s31
	v_lshl_add_u64 v[114:115], v[2:3], 0, s[10:11]
	v_lshl_add_u64 v[2:3], s[38:39], 0, v[144:145]
	s_mov_b64 s[38:39], 0x100
	v_lshl_add_u64 v[116:117], v[2:3], 0, s[38:39]
	v_mov_b32_e32 v2, 0
	s_mov_b32 s7, 4
	s_mul_hi_i32 s11, s34, 0x300
	s_mul_i32 s10, s34, 0x300
	v_or_b32_e32 v124, 0x10000, v199
	v_or_b32_e32 v125, 0x12000, v199
	v_or_b32_e32 v126, 0x18000, v200
	v_or_b32_e32 v127, 0x1c000, v200
	v_or_b32_e32 v128, 0x19000, v200
	v_or_b32_e32 v129, 0x1d000, v200
	v_or_b32_e32 v194, 0x18000, v202
	v_or_b32_e32 v195, 0x1c000, v202
	v_or_b32_e32 v201, 0x1b000, v200
	v_or_b32_e32 v202, 0x1f000, v200
	v_or_b32_e32 v203, 0x10000, v8
	v_or_b32_e32 v204, 0x10000, v10
	v_or_b32_e32 v205, 0x10000, v12
	v_or_b32_e32 v206, 0x10000, v4
	v_or_b32_e32 v207, 0x10000, v6
	v_or_b32_e32 v208, 0x10000, v7
	s_mov_b64 s[40:41], 0x80
	v_mov_b32_e32 v3, v2
	v_mov_b32_e32 v4, v2
	v_mov_b32_e32 v5, v2
	v_mov_b32_e32 v6, v2
	v_mov_b32_e32 v7, v2
	v_mov_b32_e32 v8, v2
	v_mov_b32_e32 v9, v2
	v_mov_b32_e32 v10, v2
	v_mov_b32_e32 v11, v2
	v_mov_b32_e32 v12, v2
	v_mov_b32_e32 v13, v2
	v_mov_b32_e32 v14, v2
	v_mov_b32_e32 v15, v2
	v_mov_b32_e32 v16, v2
	v_mov_b32_e32 v17, v2
	v_mov_b32_e32 v18, v2
	v_mov_b32_e32 v19, v2
	v_mov_b32_e32 v20, v2
	v_mov_b32_e32 v21, v2
	v_mov_b32_e32 v22, v2
	v_mov_b32_e32 v23, v2
	v_mov_b32_e32 v24, v2
	v_mov_b32_e32 v25, v2
	v_mov_b32_e32 v26, v2
	v_mov_b32_e32 v27, v2
	v_mov_b32_e32 v28, v2
	v_mov_b32_e32 v29, v2
	v_mov_b32_e32 v30, v2
	v_mov_b32_e32 v31, v2
	v_mov_b32_e32 v32, v2
	v_mov_b32_e32 v33, v2
	v_mov_b32_e32 v34, v2
	v_mov_b32_e32 v35, v2
	v_mov_b32_e32 v36, v2
	v_mov_b32_e32 v37, v2
	v_mov_b32_e32 v38, v2
	v_mov_b32_e32 v39, v2
	v_mov_b32_e32 v40, v2
	v_mov_b32_e32 v41, v2
	v_mov_b32_e32 v42, v2
	v_mov_b32_e32 v43, v2
	v_mov_b32_e32 v44, v2
	v_mov_b32_e32 v45, v2
	v_mov_b32_e32 v46, v2
	v_mov_b32_e32 v47, v2
	v_mov_b32_e32 v48, v2
	v_mov_b32_e32 v49, v2
	v_mov_b32_e32 v50, v2
	v_mov_b32_e32 v51, v2
	v_mov_b32_e32 v52, v2
	v_mov_b32_e32 v53, v2
	v_mov_b32_e32 v54, v2
	v_mov_b32_e32 v55, v2
	v_mov_b32_e32 v56, v2
	v_mov_b32_e32 v57, v2
	v_mov_b32_e32 v58, v2
	v_mov_b32_e32 v59, v2
	v_mov_b32_e32 v60, v2
	v_mov_b32_e32 v61, v2
	v_mov_b32_e32 v62, v2
	v_mov_b32_e32 v63, v2
	v_mov_b32_e32 v64, v2
	v_mov_b32_e32 v65, v2
	v_mov_b32_e32 v66, v2
	v_mov_b32_e32 v67, v2
	v_mov_b32_e32 v68, v2
	v_mov_b32_e32 v69, v2
	v_mov_b32_e32 v70, v2
	v_mov_b32_e32 v71, v2
	v_mov_b32_e32 v72, v2
	v_mov_b32_e32 v73, v2
	v_mov_b32_e32 v74, v2
	v_mov_b32_e32 v75, v2
	v_mov_b32_e32 v76, v2
	v_mov_b32_e32 v77, v2
	v_mov_b32_e32 v78, v2
	v_mov_b32_e32 v79, v2
	v_mov_b32_e32 v80, v2
	v_mov_b32_e32 v81, v2
	v_mov_b32_e32 v82, v2
	v_mov_b32_e32 v83, v2
	v_mov_b32_e32 v84, v2
	v_mov_b32_e32 v85, v2
	v_mov_b32_e32 v86, v2
	v_mov_b32_e32 v87, v2
	v_mov_b32_e32 v88, v2
	v_mov_b32_e32 v89, v2
	v_mov_b32_e32 v90, v2
	v_mov_b32_e32 v91, v2
	v_mov_b32_e32 v92, v2
	v_mov_b32_e32 v93, v2
	v_mov_b32_e32 v94, v2
	v_mov_b32_e32 v95, v2
	v_mov_b32_e32 v96, v2
	v_mov_b32_e32 v97, v2
	v_mov_b32_e32 v98, v2
	v_mov_b32_e32 v99, v2
	v_mov_b32_e32 v100, v2
	v_mov_b32_e32 v101, v2
	v_mov_b32_e32 v102, v2
	v_mov_b32_e32 v103, v2
	v_mov_b32_e32 v104, v2
	v_mov_b32_e32 v105, v2
	v_mov_b32_e32 v106, v2
	v_mov_b32_e32 v107, v2
	v_mov_b32_e32 v108, v2
	v_mov_b32_e32 v109, v2
	v_mov_b32_e32 v110, v2
	v_mov_b32_e32 v111, v2
	v_mov_b32_e32 v112, v2
	v_mov_b32_e32 v113, v2
	v_mov_b32_e32 v130, v2
	v_mov_b32_e32 v131, v2
	v_mov_b32_e32 v132, v2
	v_mov_b32_e32 v133, v2
	v_mov_b32_e32 v134, v2
	v_mov_b32_e32 v135, v2
	v_mov_b32_e32 v136, v2
	v_mov_b32_e32 v137, v2
	v_mov_b32_e32 v138, v2
	v_mov_b32_e32 v139, v2
	v_mov_b32_e32 v140, v2
	v_mov_b32_e32 v141, v2
	v_mov_b32_e32 v142, v2
	v_mov_b32_e32 v143, v2
	v_mov_b32_e32 v144, v2
	v_mov_b32_e32 v145, v2
	s_waitcnt vmcnt(3)
	s_branch .LBB3_4

.Lgk_hi_steady:
	s_waitcnt vmcnt(6)
	v_cvt_f16_f32_e32 v209, v150
	v_cvt_f16_f32_e32 v211, v151
	v_cvt_pk_f16_f32 v210, v150, v151
	s_add_i32 s17, s7, -1
	v_cvt_f32_f16_e32 v209, v209
	v_cvt_f32_f16_e32 v214, v211
	v_cvt_pk_f16_f32 v211, v152, v153
	v_cvt_f32_f16_e32 v212, v211
	v_cvt_f32_f16_sdwa v213, v211 dst_sel:DWORD dst_unused:UNUSED_PAD src0_sel:WORD_1
	v_sub_f32_e32 v209, v150, v209
	v_sub_f32_e32 v214, v151, v214
	v_cvt_pk_f16_f32 v214, v209, v214
	ds_write_b64 v126, v[210:211]
	v_cvt_f16_f32_e32 v209, v154
	v_cvt_f16_f32_e32 v211, v155
	v_pk_add_f32 v[212:213], v[152:153], v[212:213] neg_lo:[0,1] neg_hi:[0,1]
	v_cvt_pk_f16_f32 v210, v154, v155
	v_cvt_pk_f16_f32 v215, v212, v213
	ds_write_b64 v127, v[214:215]
	v_cvt_f32_f16_e32 v209, v209
	v_cvt_f32_f16_e32 v214, v211
	v_cvt_pk_f16_f32 v211, v156, v157
	v_cvt_f32_f16_e32 v212, v211
	v_cvt_f32_f16_sdwa v213, v211 dst_sel:DWORD dst_unused:UNUSED_PAD src0_sel:WORD_1
	v_sub_f32_e32 v209, v154, v209
	v_sub_f32_e32 v214, v155, v214
	v_cvt_pk_f16_f32 v214, v209, v214
	ds_write_b64 v128, v[210:211]
	v_cvt_f16_f32_e32 v209, v158
	v_cvt_f16_f32_e32 v211, v159
	v_pk_add_f32 v[212:213], v[156:157], v[212:213] neg_lo:[0,1] neg_hi:[0,1]
	v_cvt_pk_f16_f32 v210, v158, v159
	v_cvt_pk_f16_f32 v215, v212, v213
	ds_write_b64 v129, v[214:215]
	v_cvt_f32_f16_e32 v209, v209
	v_cvt_f32_f16_e32 v214, v211
	v_cvt_pk_f16_f32 v211, v160, v161
	v_cvt_f32_f16_e32 v212, v211
	v_cvt_f32_f16_sdwa v213, v211 dst_sel:DWORD dst_unused:UNUSED_PAD src0_sel:WORD_1
	v_sub_f32_e32 v209, v158, v209
	v_sub_f32_e32 v214, v159, v214
	ds_write_b64 v194, v[210:211]
	v_cvt_f16_f32_e32 v211, v179
	v_cvt_pk_f16_f32 v214, v209, v214
	v_cvt_f16_f32_e32 v209, v178
	v_pk_add_f32 v[212:213], v[160:161], v[212:213] neg_lo:[0,1] neg_hi:[0,1]
	v_cvt_pk_f16_f32 v210, v178, v179
	v_cvt_pk_f16_f32 v215, v212, v213
	ds_write_b64 v195, v[214:215]
	v_cvt_f32_f16_e32 v214, v211
	v_cvt_pk_f16_f32 v211, v180, v181
	v_cvt_f32_f16_e32 v209, v209
	v_cvt_f32_f16_e32 v212, v211
	v_cvt_f32_f16_sdwa v213, v211 dst_sel:DWORD dst_unused:UNUSED_PAD src0_sel:WORD_1
	v_sub_f32_e32 v214, v179, v214
	v_sub_f32_e32 v209, v178, v209
	v_cvt_pk_f16_f32 v214, v209, v214
	v_pk_add_f32 v[212:213], v[180:181], v[212:213] neg_lo:[0,1] neg_hi:[0,1]
	s_cmp_ge_i32 s17, s15
	v_cvt_pk_f16_f32 v215, v212, v213
	ds_write_b128 v124, v[146:149]
	ds_write_b128 v125, v[162:165]
	ds_write_b64 v201, v[210:211]
	ds_write_b64 v202, v[214:215]
	s_cbranch_scc1 .LBB3_6
	v_lshl_add_u64 v[150:151], v[116:117], 0, s[20:21]
	v_lshl_add_u64 v[154:155], v[114:115], 0, s[22:23]
	v_lshl_add_u64 v[158:159], v[114:115], 0, s[24:25]
	v_lshl_add_u64 v[178:179], v[114:115], 0, s[10:11]
	global_load_dwordx4 v[146:149], v[116:117], off offset:-64
	global_load_dwordx4 v[162:165], v[150:151], off offset:-64
	s_nop 0
	global_load_dwordx4 v[150:153], v[114:115], off offset:-128
	s_nop 0
	global_load_dwordx4 v[154:157], v[154:155], off offset:-128
	s_nop 0
	global_load_dwordx4 v[158:161], v[158:159], off offset:-128
	s_nop 0
	global_load_dwordx4 v[178:181], v[178:179], off offset:-128
.LBB3_6:
	ds_read_b128 v[210:213], v118
	ds_read_b128 v[214:217], v118 offset:2048
	ds_read_b128 v[218:221], v118 offset:4096
	ds_read_b128 v[222:225], v118 offset:6144
	ds_read_b128 v[230:233], v119 offset:49152
	ds_read_b128 v[226:229], v119 offset:32768
	s_add_i32 s17, s7, -2
	s_cmp_ge_i32 s17, s15
	s_waitcnt lgkmcnt(1)
	v_mfma_f32_32x32x16_f16 v[130:145], v[210:213], v[230:233], v[130:145]
	ds_read_b128 v[238:241], v119 offset:51200
	ds_read_b128 v[234:237], v119 offset:34816
	s_waitcnt lgkmcnt(2)
	v_mfma_f32_32x32x16_f16 v[130:145], v[210:213], v[226:229], v[130:145]
	s_waitcnt lgkmcnt(1)
	v_mfma_f32_32x32x16_f16 v[98:113], v[210:213], v[238:241], v[98:113]
	s_waitcnt lgkmcnt(0)
	v_mfma_f32_32x32x16_f16 v[98:113], v[210:213], v[234:237], v[98:113]
	ds_read_b128 v[210:213], v121
	v_mfma_f32_32x32x16_f16 v[82:97], v[214:217], v[230:233], v[82:97]
	v_mfma_f32_32x32x16_f16 v[82:97], v[214:217], v[226:229], v[82:97]
	v_mfma_f32_32x32x16_f16 v[66:81], v[214:217], v[238:241], v[66:81]
	v_mfma_f32_32x32x16_f16 v[66:81], v[214:217], v[234:237], v[66:81]
	ds_read_b128 v[214:217], v121 offset:2048
	v_mfma_f32_32x32x16_f16 v[50:65], v[218:221], v[230:233], v[50:65]
	v_mfma_f32_32x32x16_f16 v[50:65], v[218:221], v[226:229], v[50:65]
	v_mfma_f32_32x32x16_f16 v[34:49], v[218:221], v[238:241], v[34:49]
	v_mfma_f32_32x32x16_f16 v[34:49], v[218:221], v[234:237], v[34:49]
	ds_read_b128 v[218:221], v121 offset:4096
	v_mfma_f32_32x32x16_f16 v[18:33], v[222:225], v[230:233], v[18:33]
	ds_read_b128 v[230:233], v122 offset:49152
	v_mfma_f32_32x32x16_f16 v[18:33], v[222:225], v[226:229], v[18:33]
	ds_read_b128 v[226:229], v122 offset:32768
	v_mfma_f32_32x32x16_f16 v[2:17], v[222:225], v[238:241], v[2:17]
	ds_read_b128 v[238:241], v122 offset:51200
	v_mfma_f32_32x32x16_f16 v[2:17], v[222:225], v[234:237], v[2:17]
	ds_read_b128 v[222:225], v121 offset:6144
	ds_read_b128 v[234:237], v122 offset:34816
	s_waitcnt lgkmcnt(0)
	s_barrier
	v_mfma_f32_32x32x16_f16 v[130:145], v[210:213], v[230:233], v[130:145]
	v_mfma_f32_32x32x16_f16 v[130:145], v[210:213], v[226:229], v[130:145]
	v_mfma_f32_32x32x16_f16 v[98:113], v[210:213], v[238:241], v[98:113]
	v_mfma_f32_32x32x16_f16 v[98:113], v[210:213], v[234:237], v[98:113]
	v_mfma_f32_32x32x16_f16 v[82:97], v[214:217], v[230:233], v[82:97]
	v_mfma_f32_32x32x16_f16 v[82:97], v[214:217], v[226:229], v[82:97]
	v_mfma_f32_32x32x16_f16 v[66:81], v[214:217], v[238:241], v[66:81]
	v_mfma_f32_32x32x16_f16 v[66:81], v[214:217], v[234:237], v[66:81]
	v_mfma_f32_32x32x16_f16 v[50:65], v[218:221], v[230:233], v[50:65]
	v_mfma_f32_32x32x16_f16 v[50:65], v[218:221], v[226:229], v[50:65]
	v_mfma_f32_32x32x16_f16 v[34:49], v[218:221], v[238:241], v[34:49]
	v_mfma_f32_32x32x16_f16 v[34:49], v[218:221], v[234:237], v[34:49]
	v_mfma_f32_32x32x16_f16 v[18:33], v[222:225], v[230:233], v[18:33]
	v_mfma_f32_32x32x16_f16 v[18:33], v[222:225], v[226:229], v[18:33]
	v_mfma_f32_32x32x16_f16 v[2:17], v[222:225], v[238:241], v[2:17]
	v_mfma_f32_32x32x16_f16 v[2:17], v[222:225], v[234:237], v[2:17]
	s_cbranch_scc1 .LBB3_3
	s_waitcnt vmcnt(6)
	v_cvt_f16_f32_e32 v209, v174
	v_cvt_f16_f32_e32 v211, v175
	v_cvt_f16_f32_e32 v216, v183
	v_cvt_pk_f16_f32 v210, v174, v175
	v_cvt_f32_f16_e32 v209, v209
	v_cvt_f32_f16_e32 v214, v211
	v_cvt_pk_f16_f32 v211, v176, v177
	v_cvt_f32_f16_e32 v212, v211
	v_sub_f32_e32 v209, v174, v209
	v_sub_f32_e32 v214, v175, v214
	v_cvt_pk_f16_f32 v214, v209, v214
	v_cvt_f16_f32_e32 v209, v182
	v_cvt_f32_f16_sdwa v213, v211 dst_sel:DWORD dst_unused:UNUSED_PAD src0_sel:WORD_1
	v_cvt_f32_f16_e32 v218, v216
	s_cmp_ge_i32 s7, s15
	v_cvt_f32_f16_e32 v209, v209
	v_pk_add_f32 v[212:213], v[176:177], v[212:213] neg_lo:[0,1] neg_hi:[0,1]
	v_sub_f32_e32 v218, v183, v218
	v_cvt_pk_f16_f32 v215, v212, v213
	v_cvt_pk_f16_f32 v213, v184, v185
	v_cvt_f32_f16_e32 v216, v213
	v_cvt_f32_f16_sdwa v217, v213 dst_sel:DWORD dst_unused:UNUSED_PAD src0_sel:WORD_1
	v_cvt_pk_f16_f32 v212, v182, v183
	v_sub_f32_e32 v209, v182, v209
	v_cvt_pk_f16_f32 v218, v209, v218
	ds_write2st64_b64 v200, v[210:211], v[212:213] offset0:64 offset1:72
	v_cvt_f16_f32_e32 v209, v186
	v_cvt_f16_f32_e32 v211, v187
	v_pk_add_f32 v[216:217], v[184:185], v[216:217] neg_lo:[0,1] neg_hi:[0,1]
	v_cvt_pk_f16_f32 v210, v186, v187
	v_cvt_pk_f16_f32 v219, v216, v217
	ds_write2st64_b64 v200, v[214:215], v[218:219] offset0:96 offset1:104
	v_cvt_f32_f16_e32 v209, v209
	v_cvt_f32_f16_e32 v214, v211
	v_cvt_pk_f16_f32 v211, v188, v189
	v_cvt_f32_f16_e32 v212, v211
	v_cvt_f32_f16_sdwa v213, v211 dst_sel:DWORD dst_unused:UNUSED_PAD src0_sel:WORD_1
	v_sub_f32_e32 v209, v186, v209
	v_sub_f32_e32 v214, v187, v214
	v_cvt_pk_f16_f32 v214, v209, v214
	v_cvt_f16_f32_e32 v209, v190
	v_cvt_f16_f32_e32 v216, v191
	v_pk_add_f32 v[212:213], v[188:189], v[212:213] neg_lo:[0,1] neg_hi:[0,1]
	ds_write_b128 v199, v[166:169]
	v_cvt_pk_f16_f32 v215, v212, v213
	v_cvt_pk_f16_f32 v213, v192, v193
	v_cvt_f32_f16_e32 v209, v209
	v_cvt_f32_f16_e32 v218, v216
	v_cvt_f32_f16_e32 v216, v213
	v_cvt_f32_f16_sdwa v217, v213 dst_sel:DWORD dst_unused:UNUSED_PAD src0_sel:WORD_1
	v_sub_f32_e32 v209, v190, v209
	v_sub_f32_e32 v218, v191, v218
	v_cvt_pk_f16_f32 v212, v190, v191
	v_pk_add_f32 v[216:217], v[192:193], v[216:217] neg_lo:[0,1] neg_hi:[0,1]
	v_cvt_pk_f16_f32 v218, v209, v218
	v_cvt_pk_f16_f32 v219, v216, v217
	ds_write_b128 v199, v[170:173] offset:8192
	ds_write2st64_b64 v200, v[210:211], v[212:213] offset0:80 offset1:88
	ds_write2st64_b64 v200, v[214:215], v[218:219] offset0:112 offset1:120
	s_cbranch_scc1 .LBB3_3
	v_lshl_add_u64 v[170:171], v[116:117], 0, s[20:21]
	v_lshl_add_u64 v[182:183], v[114:115], 0, s[22:23]
	v_lshl_add_u64 v[186:187], v[114:115], 0, s[24:25]
	v_lshl_add_u64 v[190:191], v[114:115], 0, s[10:11]
	global_load_dwordx4 v[166:169], v[116:117], off
	s_nop 0
	global_load_dwordx4 v[170:173], v[170:171], off
	s_nop 0
	global_load_dwordx4 v[174:177], v[114:115], off
	s_nop 0
	global_load_dwordx4 v[182:185], v[182:183], off
	s_nop 0
	global_load_dwordx4 v[186:189], v[186:187], off
	s_nop 0
	global_load_dwordx4 v[190:193], v[190:191], off
	s_branch .LBB3_3

.Lgk_lo_steady:
	s_waitcnt vmcnt(6)
	v_cvt_f16_f32_e32 v209, v150
	s_add_i32 s28, s35, -1
	s_cmp_ge_i32 s28, s15
	s_waitcnt lgkmcnt(0)
	v_mfma_f32_32x32x16_f16 v[114:129], v[210:213], v[230:233], v[114:129]
	ds_read_b128 v[238:241], v135 offset:51200
	ds_read_b128 v[234:237], v135 offset:34816
	v_cvt_f32_f16_e32 v209, v209
	v_sub_f32_e32 v209, v150, v209
	v_mfma_f32_32x32x16_f16 v[114:129], v[210:213], v[226:229], v[114:129]
	s_waitcnt lgkmcnt(1)
	v_mfma_f32_32x32x16_f16 v[98:113], v[210:213], v[238:241], v[98:113]
	s_waitcnt lgkmcnt(0)
	v_mfma_f32_32x32x16_f16 v[98:113], v[210:213], v[234:237], v[98:113]
	ds_read_b128 v[210:213], v137
	v_mfma_f32_32x32x16_f16 v[82:97], v[214:217], v[230:233], v[82:97]
	v_mfma_f32_32x32x16_f16 v[82:97], v[214:217], v[226:229], v[82:97]
	v_mfma_f32_32x32x16_f16 v[66:81], v[214:217], v[238:241], v[66:81]
	v_mfma_f32_32x32x16_f16 v[66:81], v[214:217], v[234:237], v[66:81]
	ds_read_b128 v[214:217], v137 offset:2048
	v_mfma_f32_32x32x16_f16 v[50:65], v[218:221], v[230:233], v[50:65]
	v_mfma_f32_32x32x16_f16 v[50:65], v[218:221], v[226:229], v[50:65]
	v_mfma_f32_32x32x16_f16 v[34:49], v[218:221], v[238:241], v[34:49]
	v_mfma_f32_32x32x16_f16 v[34:49], v[218:221], v[234:237], v[34:49]
	ds_read_b128 v[218:221], v137 offset:4096
	v_mfma_f32_32x32x16_f16 v[18:33], v[222:225], v[230:233], v[18:33]
	ds_read_b128 v[230:233], v138 offset:49152
	v_mfma_f32_32x32x16_f16 v[18:33], v[222:225], v[226:229], v[18:33]
	ds_read_b128 v[226:229], v138 offset:32768
	v_mfma_f32_32x32x16_f16 v[2:17], v[222:225], v[238:241], v[2:17]
	ds_read_b128 v[238:241], v138 offset:51200
	v_mfma_f32_32x32x16_f16 v[2:17], v[222:225], v[234:237], v[2:17]
	ds_read_b128 v[222:225], v137 offset:6144
	ds_read_b128 v[234:237], v138 offset:34816
	s_waitcnt lgkmcnt(4)
	v_mfma_f32_32x32x16_f16 v[114:129], v[210:213], v[230:233], v[114:129]
	ds_write_b128 v140, v[146:149]
	ds_write_b128 v141, v[162:165]
	s_waitcnt lgkmcnt(5)
	v_mfma_f32_32x32x16_f16 v[114:129], v[210:213], v[226:229], v[114:129]
	s_waitcnt lgkmcnt(4)
	v_mfma_f32_32x32x16_f16 v[98:113], v[210:213], v[238:241], v[98:113]
	s_waitcnt lgkmcnt(2)
	v_mfma_f32_32x32x16_f16 v[98:113], v[210:213], v[234:237], v[98:113]
	v_cvt_f16_f32_e32 v211, v151
	v_cvt_pk_f16_f32 v210, v150, v151
	v_cvt_f32_f16_e32 v211, v211
	v_sub_f32_e32 v211, v151, v211
	v_cvt_pk_f16_f32 v212, v209, v211
	v_cvt_pk_f16_f32 v211, v152, v153
	ds_write_b64 v142, v[210:211]
	v_mfma_f32_32x32x16_f16 v[82:97], v[214:217], v[230:233], v[82:97]
	v_cvt_f16_f32_e32 v209, v154
	v_cvt_pk_f16_f32 v210, v154, v155
	v_cvt_f32_f16_e32 v209, v209
	v_sub_f32_e32 v209, v154, v209
	v_mfma_f32_32x32x16_f16 v[82:97], v[214:217], v[226:229], v[82:97]
	v_mfma_f32_32x32x16_f16 v[66:81], v[214:217], v[238:241], v[66:81]
	v_mfma_f32_32x32x16_f16 v[66:81], v[214:217], v[234:237], v[66:81]
	v_cvt_f32_f16_e32 v214, v211
	v_cvt_f32_f16_sdwa v215, v211 dst_sel:DWORD dst_unused:UNUSED_PAD src0_sel:WORD_1
	v_cvt_f16_f32_e32 v211, v155
	v_add_f32_e64 v214, v152, -v214
	v_add_f32_e64 v215, v153, -v215
	v_cvt_f32_f16_e32 v211, v211
	v_cvt_pk_f16_f32 v213, v214, v215
	ds_write_b64 v143, v[212:213]
	v_sub_f32_e32 v211, v155, v211
	v_cvt_pk_f16_f32 v212, v209, v211
	v_cvt_pk_f16_f32 v211, v156, v157
	v_cvt_f32_f16_e32 v214, v211
	v_cvt_f32_f16_sdwa v215, v211 dst_sel:DWORD dst_unused:UNUSED_PAD src0_sel:WORD_1
	ds_write_b64 v144, v[210:211]
	v_cvt_f16_f32_e32 v209, v158
	v_cvt_f16_f32_e32 v211, v159
	v_pk_add_f32 v[214:215], v[156:157], v[214:215] neg_lo:[0,1] neg_hi:[0,1]
	v_mfma_f32_32x32x16_f16 v[50:65], v[218:221], v[230:233], v[50:65]
	v_cvt_f32_f16_e32 v209, v209
	v_cvt_f32_f16_e32 v211, v211
	v_cvt_pk_f16_f32 v213, v214, v215
	ds_write_b64 v145, v[212:213]
	v_sub_f32_e32 v209, v158, v209
	v_sub_f32_e32 v211, v159, v211
	v_cvt_pk_f16_f32 v210, v158, v159
	v_cvt_pk_f16_f32 v212, v209, v211
	v_cvt_pk_f16_f32 v211, v160, v161
	v_cvt_f32_f16_e32 v214, v211
	v_cvt_f32_f16_sdwa v215, v211 dst_sel:DWORD dst_unused:UNUSED_PAD src0_sel:WORD_1
	ds_write_b64 v194, v[210:211]
	v_cvt_f16_f32_e32 v209, v178
	v_cvt_f16_f32_e32 v211, v179
	v_pk_add_f32 v[214:215], v[160:161], v[214:215] neg_lo:[0,1] neg_hi:[0,1]
	v_mfma_f32_32x32x16_f16 v[50:65], v[218:221], v[226:229], v[50:65]
	v_cvt_f32_f16_e32 v209, v209
	v_cvt_f32_f16_e32 v211, v211
	v_cvt_pk_f16_f32 v213, v214, v215
	ds_write_b64 v195, v[212:213]
	v_sub_f32_e32 v209, v178, v209
	v_sub_f32_e32 v211, v179, v211
	v_cvt_pk_f16_f32 v210, v178, v179
	v_cvt_pk_f16_f32 v212, v209, v211
	v_cvt_pk_f16_f32 v211, v180, v181
	ds_write_b64 v201, v[210:211]
	v_mfma_f32_32x32x16_f16 v[34:49], v[218:221], v[238:241], v[34:49]
	v_cvt_f32_f16_e32 v214, v211
	v_cvt_f32_f16_sdwa v215, v211 dst_sel:DWORD dst_unused:UNUSED_PAD src0_sel:WORD_1
	v_add_f32_e64 v214, v180, -v214
	v_add_f32_e64 v215, v181, -v215
	v_cvt_pk_f16_f32 v213, v214, v215
	ds_write_b64 v202, v[212:213]
	v_mfma_f32_32x32x16_f16 v[34:49], v[218:221], v[234:237], v[34:49]
	v_mfma_f32_32x32x16_f16 v[18:33], v[222:225], v[230:233], v[18:33]
	v_mfma_f32_32x32x16_f16 v[18:33], v[222:225], v[226:229], v[18:33]
	v_mfma_f32_32x32x16_f16 v[2:17], v[222:225], v[238:241], v[2:17]
	v_mfma_f32_32x32x16_f16 v[2:17], v[222:225], v[234:237], v[2:17]
	s_cbranch_scc1 .LBB3_17
	v_lshl_add_u64 v[150:151], v[132:133], 0, s[20:21]
	v_lshl_add_u64 v[154:155], v[130:131], 0, s[22:23]
	v_lshl_add_u64 v[158:159], v[130:131], 0, s[24:25]
	v_lshl_add_u64 v[178:179], v[130:131], 0, s[0:1]
	global_load_dwordx4 v[146:149], v[132:133], off offset:-64
	global_load_dwordx4 v[162:165], v[150:151], off offset:-64
	s_nop 0
	global_load_dwordx4 v[150:153], v[130:131], off offset:-128
	s_nop 0
	global_load_dwordx4 v[154:157], v[154:155], off offset:-128
	s_nop 0
	global_load_dwordx4 v[158:161], v[158:159], off offset:-128
	s_nop 0
	global_load_dwordx4 v[178:181], v[178:179], off offset:-128
.LBB3_17:
	v_or_b32_e32 v209, 0x10000, v134
	s_waitcnt lgkmcnt(0)
	s_barrier
	ds_read_b128 v[210:213], v209
	v_or_b32_e32 v209, 0x18000, v135
	ds_read_b128 v[214:217], v203
	ds_read_b128 v[218:221], v204
	ds_read_b128 v[222:225], v205
	ds_read_b128 v[226:229], v209
	v_add_u32_e32 v209, 0x1c000, v135
	ds_read_b128 v[230:233], v209
	s_waitcnt lgkmcnt(0)
	v_mfma_f32_32x32x16_f16 v[114:129], v[210:213], v[230:233], v[114:129]
	v_or_b32_e32 v209, 0x18000, v136
	ds_read_b128 v[234:237], v209
	v_add_u32_e32 v209, 0x1c000, v136
	ds_read_b128 v[238:241], v209
	v_or_b32_e32 v209, 0x10000, v137
	s_add_i32 s28, s35, -2
	s_cmp_ge_i32 s28, s15
	v_mfma_f32_32x32x16_f16 v[114:129], v[210:213], v[226:229], v[114:129]
	s_waitcnt lgkmcnt(0)
	v_mfma_f32_32x32x16_f16 v[98:113], v[210:213], v[238:241], v[98:113]
	v_mfma_f32_32x32x16_f16 v[98:113], v[210:213], v[234:237], v[98:113]
	ds_read_b128 v[210:213], v209
	v_or_b32_e32 v209, 0x18000, v138
	v_mfma_f32_32x32x16_f16 v[82:97], v[214:217], v[230:233], v[82:97]
	v_mfma_f32_32x32x16_f16 v[82:97], v[214:217], v[226:229], v[82:97]
	v_mfma_f32_32x32x16_f16 v[66:81], v[214:217], v[238:241], v[66:81]
	v_mfma_f32_32x32x16_f16 v[66:81], v[214:217], v[234:237], v[66:81]
	ds_read_b128 v[214:217], v206
	v_mfma_f32_32x32x16_f16 v[50:65], v[218:221], v[230:233], v[50:65]
	v_mfma_f32_32x32x16_f16 v[50:65], v[218:221], v[226:229], v[50:65]
	v_mfma_f32_32x32x16_f16 v[34:49], v[218:221], v[238:241], v[34:49]
	v_mfma_f32_32x32x16_f16 v[34:49], v[218:221], v[234:237], v[34:49]
	ds_read_b128 v[218:221], v207
	v_mfma_f32_32x32x16_f16 v[18:33], v[222:225], v[230:233], v[18:33]
	v_mfma_f32_32x32x16_f16 v[18:33], v[222:225], v[226:229], v[18:33]
	ds_read_b128 v[226:229], v209
	v_add_u32_e32 v209, 0x1c000, v138
	ds_read_b128 v[230:233], v209
	v_or_b32_e32 v209, 0x18000, v139
	v_mfma_f32_32x32x16_f16 v[2:17], v[222:225], v[238:241], v[2:17]
	v_mfma_f32_32x32x16_f16 v[2:17], v[222:225], v[234:237], v[2:17]
	ds_read_b128 v[222:225], v208
	ds_read_b128 v[234:237], v209
	v_add_u32_e32 v209, 0x1c000, v139
	s_waitcnt lgkmcnt(2)
	v_mfma_f32_32x32x16_f16 v[114:129], v[210:213], v[230:233], v[114:129]
	ds_read_b128 v[238:241], v209
	v_mfma_f32_32x32x16_f16 v[114:129], v[210:213], v[226:229], v[114:129]
	s_waitcnt lgkmcnt(0)
	v_mfma_f32_32x32x16_f16 v[98:113], v[210:213], v[238:241], v[98:113]
	v_mfma_f32_32x32x16_f16 v[98:113], v[210:213], v[234:237], v[98:113]
	v_mfma_f32_32x32x16_f16 v[82:97], v[214:217], v[230:233], v[82:97]
	v_mfma_f32_32x32x16_f16 v[82:97], v[214:217], v[226:229], v[82:97]
	v_mfma_f32_32x32x16_f16 v[66:81], v[214:217], v[238:241], v[66:81]
	v_mfma_f32_32x32x16_f16 v[66:81], v[214:217], v[234:237], v[66:81]
	v_mfma_f32_32x32x16_f16 v[50:65], v[218:221], v[230:233], v[50:65]
	v_mfma_f32_32x32x16_f16 v[50:65], v[218:221], v[226:229], v[50:65]
	v_mfma_f32_32x32x16_f16 v[34:49], v[218:221], v[238:241], v[34:49]
	v_mfma_f32_32x32x16_f16 v[34:49], v[218:221], v[234:237], v[34:49]
	v_mfma_f32_32x32x16_f16 v[18:33], v[222:225], v[230:233], v[18:33]
	v_mfma_f32_32x32x16_f16 v[18:33], v[222:225], v[226:229], v[18:33]
	v_mfma_f32_32x32x16_f16 v[2:17], v[222:225], v[238:241], v[2:17]
	v_mfma_f32_32x32x16_f16 v[2:17], v[222:225], v[234:237], v[2:17]
	s_cbranch_scc1 .LBB3_14
	s_waitcnt vmcnt(6)
	v_cvt_f16_f32_e32 v209, v174
	v_cvt_f16_f32_e32 v211, v175
	v_cvt_f16_f32_e32 v216, v183
	v_cvt_pk_f16_f32 v210, v174, v175
	v_cvt_f32_f16_e32 v209, v209
	v_cvt_f32_f16_e32 v214, v211
	v_cvt_pk_f16_f32 v211, v176, v177
	v_cvt_f32_f16_e32 v212, v211
	v_sub_f32_e32 v209, v174, v209
	v_sub_f32_e32 v214, v175, v214
	v_cvt_pk_f16_f32 v214, v209, v214
	v_cvt_f16_f32_e32 v209, v182
	v_cvt_f32_f16_sdwa v213, v211 dst_sel:DWORD dst_unused:UNUSED_PAD src0_sel:WORD_1
	v_cvt_f32_f16_e32 v218, v216
	s_cmp_ge_i32 s35, s15
	v_cvt_f32_f16_e32 v209, v209
	v_pk_add_f32 v[212:213], v[176:177], v[212:213] neg_lo:[0,1] neg_hi:[0,1]
	v_sub_f32_e32 v218, v183, v218
	v_cvt_pk_f16_f32 v215, v212, v213
	v_cvt_pk_f16_f32 v213, v184, v185
	v_cvt_f32_f16_e32 v216, v213
	v_cvt_f32_f16_sdwa v217, v213 dst_sel:DWORD dst_unused:UNUSED_PAD src0_sel:WORD_1
	v_cvt_pk_f16_f32 v212, v182, v183
	v_sub_f32_e32 v209, v182, v209
	v_cvt_pk_f16_f32 v218, v209, v218
	ds_write2st64_b64 v200, v[210:211], v[212:213] offset0:64 offset1:72
	v_cvt_f16_f32_e32 v209, v186
	v_cvt_f16_f32_e32 v211, v187
	v_pk_add_f32 v[216:217], v[184:185], v[216:217] neg_lo:[0,1] neg_hi:[0,1]
	v_cvt_pk_f16_f32 v210, v186, v187
	v_cvt_pk_f16_f32 v219, v216, v217
	ds_write2st64_b64 v200, v[214:215], v[218:219] offset0:96 offset1:104
	v_cvt_f32_f16_e32 v209, v209
	v_cvt_f32_f16_e32 v214, v211
	v_cvt_pk_f16_f32 v211, v188, v189
	v_cvt_f32_f16_e32 v212, v211
	v_cvt_f32_f16_sdwa v213, v211 dst_sel:DWORD dst_unused:UNUSED_PAD src0_sel:WORD_1
	v_sub_f32_e32 v209, v186, v209
	v_sub_f32_e32 v214, v187, v214
	v_cvt_pk_f16_f32 v214, v209, v214
	v_cvt_f16_f32_e32 v209, v190
	v_cvt_f16_f32_e32 v216, v191
	v_pk_add_f32 v[212:213], v[188:189], v[212:213] neg_lo:[0,1] neg_hi:[0,1]
	ds_write_b128 v199, v[166:169]
	v_cvt_pk_f16_f32 v215, v212, v213
	v_cvt_pk_f16_f32 v213, v192, v193
	v_cvt_f32_f16_e32 v209, v209
	v_cvt_f32_f16_e32 v218, v216
	v_cvt_f32_f16_e32 v216, v213
	v_cvt_f32_f16_sdwa v217, v213 dst_sel:DWORD dst_unused:UNUSED_PAD src0_sel:WORD_1
	v_sub_f32_e32 v209, v190, v209
	v_sub_f32_e32 v218, v191, v218
	v_cvt_pk_f16_f32 v212, v190, v191
	v_pk_add_f32 v[216:217], v[192:193], v[216:217] neg_lo:[0,1] neg_hi:[0,1]
	v_cvt_pk_f16_f32 v218, v209, v218
	v_cvt_pk_f16_f32 v219, v216, v217
	ds_write_b128 v199, v[170:173] offset:8192
	ds_write2st64_b64 v200, v[210:211], v[212:213] offset0:80 offset1:88
	ds_write2st64_b64 v200, v[214:215], v[218:219] offset0:112 offset1:120
	s_cbranch_scc1 .LBB3_14
	v_lshl_add_u64 v[170:171], v[132:133], 0, s[20:21]
	v_lshl_add_u64 v[182:183], v[130:131], 0, s[22:23]
	v_lshl_add_u64 v[186:187], v[130:131], 0, s[24:25]
	v_lshl_add_u64 v[190:191], v[130:131], 0, s[0:1]
	global_load_dwordx4 v[166:169], v[132:133], off
	s_nop 0
	global_load_dwordx4 v[170:173], v[170:171], off
	s_nop 0
	global_load_dwordx4 v[174:177], v[130:131], off
	s_nop 0
	global_load_dwordx4 v[182:185], v[182:183], off
	s_nop 0
	global_load_dwordx4 v[186:189], v[186:187], off
	s_nop 0
	global_load_dwordx4 v[190:193], v[190:191], off
	s_branch .LBB3_14

.LBB4_4:
	global_load_dwordx4 v[22:25], v[26:27], off offset:-12
	global_load_dwordx4 v[18:21], v[26:27], off offset:4
	global_load_dwordx4 v[14:17], v[26:27], off offset:20
	global_load_dwordx4 v[10:13], v[26:27], off offset:36
	v_lshl_add_u64 v[176:177], v[28:29], 0, s[22:23]
	global_load_dwordx4 v[30:33], v[176:177], off nt
	global_load_dwordx4 v[34:37], v[176:177], off offset:1024 nt
	global_load_dwordx4 v[38:41], v[176:177], off offset:2048 nt
	global_load_dwordx4 v[42:45], v[176:177], off offset:3072 nt
	global_load_dwordx4 v[92:95], v[26:27], off offset:52
	global_load_dwordx4 v[88:91], v[26:27], off offset:68
	global_load_dwordx4 v[84:87], v[26:27], off offset:84
	global_load_dwordx4 v[80:83], v[26:27], off offset:100
	s_add_u32 s22, s22, 0x1000
	s_addc_u32 s23, s23, 0
	v_lshl_add_u64 v[178:179], v[28:29], 0, s[22:23]
	global_load_dwordx4 v[96:99], v[178:179], off nt
	global_load_dwordx4 v[100:103], v[178:179], off offset:1024 nt
	global_load_dwordx4 v[104:107], v[178:179], off offset:2048 nt
	global_load_dwordx4 v[108:111], v[178:179], off offset:3072 nt
	global_load_dwordx4 v[124:127], v[26:27], off offset:116
	global_load_dwordx4 v[120:123], v[26:27], off offset:132
	global_load_dwordx4 v[116:119], v[26:27], off offset:148
	global_load_dwordx4 v[112:115], v[26:27], off offset:164
	s_add_u32 s22, s22, 0x1000
	s_addc_u32 s23, s23, 0
	v_lshl_add_u64 v[180:181], v[28:29], 0, s[22:23]
	global_load_dwordx4 v[128:131], v[180:181], off nt
	global_load_dwordx4 v[132:135], v[180:181], off offset:1024 nt
	global_load_dwordx4 v[136:139], v[180:181], off offset:2048 nt
	global_load_dwordx4 v[140:143], v[180:181], off offset:3072 nt
	global_load_dwordx4 v[156:159], v[26:27], off offset:180
	global_load_dwordx4 v[152:155], v[26:27], off offset:196
	global_load_dwordx4 v[148:151], v[26:27], off offset:212
	global_load_dwordx4 v[144:147], v[26:27], off offset:228
	s_add_u32 s22, s22, 0x1000
	s_addc_u32 s23, s23, 0
	v_lshl_add_u64 v[182:183], v[28:29], 0, s[22:23]
	global_load_dwordx4 v[160:163], v[182:183], off nt
	global_load_dwordx4 v[164:167], v[182:183], off offset:1024 nt
	global_load_dwordx4 v[168:171], v[182:183], off offset:2048 nt
	global_load_dwordx4 v[172:175], v[182:183], off offset:3072 nt
	s_waitcnt vmcnt(31)
	v_max_f32_e32 v46, v24, v24
	v_max_f32_e32 v47, v22, v22
	s_waitcnt vmcnt(30)
	v_max_f32_e32 v50, v20, v20
	v_max_f32_e32 v51, v18, v18
	s_waitcnt vmcnt(29)
	v_max_f32_e32 v54, v16, v16
	v_max_f32_e32 v55, v14, v14
	s_waitcnt vmcnt(28)
	v_max_f32_e32 v58, v12, v12
	v_max_f32_e32 v59, v10, v10
	v_max_f32_e32 v62, v47, v46
	v_max_f32_e32 v63, v51, v50
	v_max_f32_e32 v64, v55, v54
	v_max_f32_e32 v65, v59, v58
	v_sub_f32_e32 v22, v22, v62
	v_sub_f32_e32 v62, v24, v62
	v_mov_b32_e32 v24, v23
	v_sub_f32_e32 v18, v18, v63
	v_sub_f32_e32 v23, v20, v63
	v_mov_b32_e32 v20, v19
	v_sub_f32_e32 v14, v14, v64
	v_sub_f32_e32 v19, v16, v64
	v_mov_b32_e32 v16, v15
	v_sub_f32_e32 v10, v10, v65
	v_sub_f32_e32 v15, v12, v65
	v_mov_b32_e32 v12, v11
	v_mul_f32_e32 v11, 0x3fb8aa3b, v22
	v_mul_f32_e32 v22, 0x3fb8aa3b, v62
	v_mul_f32_e32 v18, 0x3fb8aa3b, v18
	v_mul_f32_e32 v23, 0x3fb8aa3b, v23
	v_mul_f32_e32 v62, 0x3fb8aa3b, v14
	v_mul_f32_e32 v19, 0x3fb8aa3b, v19
	v_mul_f32_e32 v63, 0x3fb8aa3b, v10
	v_mul_f32_e32 v64, 0x3fb8aa3b, v15
	v_exp_f32_e32 v10, v11
	v_exp_f32_e32 v11, v22
	v_exp_f32_e32 v14, v18
	v_exp_f32_e32 v15, v23
	v_exp_f32_e32 v18, v62
	v_exp_f32_e32 v19, v19
	v_exp_f32_e32 v22, v63
	v_exp_f32_e32 v23, v64
	v_pk_mul_f32 v[24:25], v[24:25], v[10:11]
	v_cndmask_b32_e64 v62, v11, v10, s[4:5]
	v_pk_mul_f32 v[10:11], v[20:21], v[14:15]
	v_cndmask_b32_e64 v20, v15, v14, s[4:5]
	v_pk_mul_f32 v[14:15], v[16:17], v[18:19]
	v_cndmask_b32_e64 v16, v19, v18, s[4:5]
	v_pk_mul_f32 v[12:13], v[12:13], v[22:23]
	v_add_f32_e32 v18, v24, v25
	v_add_f32_e32 v10, v10, v11
	v_add_f32_e32 v12, v12, v13
	v_div_scale_f32 v13, s[6:7], v18, v18, 1.0
	v_add_f32_e32 v11, v14, v15
	v_div_scale_f32 v15, s[6:7], v10, v10, 1.0
	v_rcp_f32_e32 v25, v13
	v_div_scale_f32 v21, s[8:9], v11, v11, 1.0
	v_rcp_f32_e32 v63, v15
	v_cndmask_b32_e64 v17, v23, v22, s[4:5]
	v_div_scale_f32 v23, s[10:11], v12, v12, 1.0
	v_rcp_f32_e32 v64, v21
	v_rcp_f32_e32 v65, v23
	v_fma_f32 v66, -v13, v25, 1.0
	v_div_scale_f32 v14, vcc, 1.0, v18, 1.0
	v_fma_f32 v67, -v15, v63, 1.0
	v_fmac_f32_e32 v25, v66, v25
	v_div_scale_f32 v19, s[6:7], 1.0, v10, 1.0
	v_fma_f32 v68, -v21, v64, 1.0
	v_fmac_f32_e32 v63, v67, v63
	v_mul_f32_e32 v66, v14, v25
	v_div_scale_f32 v22, s[8:9], 1.0, v11, 1.0
	v_fma_f32 v69, -v23, v65, 1.0
	v_fmac_f32_e32 v64, v68, v64
	v_mul_f32_e32 v67, v19, v63
	v_fma_f32 v70, -v13, v66, v14
	v_div_scale_f32 v24, s[10:11], 1.0, v12, 1.0
	v_fmac_f32_e32 v65, v69, v65
	v_mul_f32_e32 v68, v22, v64
	v_fma_f32 v71, -v15, v67, v19
	v_fmac_f32_e32 v66, v70, v25
	v_mul_f32_e32 v69, v24, v65
	v_fma_f32 v72, -v21, v68, v22
	v_fmac_f32_e32 v67, v71, v63
	v_fma_f32 v13, -v13, v66, v14
	s_waitcnt vmcnt(27)
	v_cvt_f32_f16_e32 v46, v30
	v_cvt_f32_f16_sdwa v47, v30 dst_sel:DWORD dst_unused:UNUSED_PAD src0_sel:WORD_1
	v_cvt_f32_f16_e32 v30, v31
	v_cvt_f32_f16_sdwa v31, v31 dst_sel:DWORD dst_unused:UNUSED_PAD src0_sel:WORD_1
	v_cvt_f32_f16_e32 v48, v32
	v_cvt_f32_f16_sdwa v49, v32 dst_sel:DWORD dst_unused:UNUSED_PAD src0_sel:WORD_1
	v_cvt_f32_f16_e32 v32, v33
	v_cvt_f32_f16_sdwa v33, v33 dst_sel:DWORD dst_unused:UNUSED_PAD src0_sel:WORD_1
	v_fma_f32 v73, -v23, v69, v24
	v_fmac_f32_e32 v68, v72, v64
	v_fma_f32 v14, -v15, v67, v19
	v_div_fmas_f32 v13, v13, v25, v66
	s_mov_b64 vcc, s[6:7]
	s_waitcnt vmcnt(26)
	v_cvt_f32_f16_e32 v50, v34
	v_cvt_f32_f16_sdwa v51, v34 dst_sel:DWORD dst_unused:UNUSED_PAD src0_sel:WORD_1
	v_cvt_f32_f16_e32 v34, v35
	v_cvt_f32_f16_sdwa v35, v35 dst_sel:DWORD dst_unused:UNUSED_PAD src0_sel:WORD_1
	v_cvt_f32_f16_e32 v52, v36
	v_cvt_f32_f16_sdwa v53, v36 dst_sel:DWORD dst_unused:UNUSED_PAD src0_sel:WORD_1
	v_cvt_f32_f16_e32 v36, v37
	v_cvt_f32_f16_sdwa v37, v37 dst_sel:DWORD dst_unused:UNUSED_PAD src0_sel:WORD_1
	v_fmac_f32_e32 v69, v73, v65
	v_fma_f32 v15, -v21, v68, v22
	v_div_fixup_f32 v13, v13, v18, 1.0
	v_div_fmas_f32 v14, v14, v63, v67
	s_mov_b64 vcc, s[8:9]
	s_waitcnt vmcnt(25)
	v_cvt_f32_f16_e32 v54, v38
	v_cvt_f32_f16_sdwa v55, v38 dst_sel:DWORD dst_unused:UNUSED_PAD src0_sel:WORD_1
	v_cvt_f32_f16_e32 v38, v39
	v_cvt_f32_f16_sdwa v39, v39 dst_sel:DWORD dst_unused:UNUSED_PAD src0_sel:WORD_1
	v_cvt_f32_f16_e32 v56, v40
	v_cvt_f32_f16_sdwa v57, v40 dst_sel:DWORD dst_unused:UNUSED_PAD src0_sel:WORD_1
	v_cvt_f32_f16_e32 v40, v41
	v_cvt_f32_f16_sdwa v41, v41 dst_sel:DWORD dst_unused:UNUSED_PAD src0_sel:WORD_1
	v_fma_f32 v19, -v23, v69, v24
	v_mul_f32_e32 v13, v62, v13
	v_div_fixup_f32 v14, v14, v10, 1.0
	v_div_fmas_f32 v15, v15, v64, v68
	s_mov_b64 vcc, s[10:11]
	s_waitcnt vmcnt(24)
	v_cvt_f32_f16_e32 v58, v42
	v_cvt_f32_f16_sdwa v59, v42 dst_sel:DWORD dst_unused:UNUSED_PAD src0_sel:WORD_1
	v_cvt_f32_f16_e32 v42, v43
	v_cvt_f32_f16_sdwa v43, v43 dst_sel:DWORD dst_unused:UNUSED_PAD src0_sel:WORD_1
	v_cvt_f32_f16_e32 v60, v44
	v_cvt_f32_f16_sdwa v61, v44 dst_sel:DWORD dst_unused:UNUSED_PAD src0_sel:WORD_1
	v_cvt_f32_f16_e32 v44, v45
	v_cvt_f32_f16_sdwa v45, v45 dst_sel:DWORD dst_unused:UNUSED_PAD src0_sel:WORD_1
	v_mul_f32_e32 v10, 0x38800000, v13
	v_mul_f32_e32 v13, v20, v14
	v_div_fixup_f32 v11, v15, v11, 1.0
	v_div_fmas_f32 v14, v19, v65, v69
	v_pk_fma_f32 v[6:7], v[10:11], v[46:47], v[6:7] op_sel_hi:[0,1,1]
	v_pk_fma_f32 v[8:9], v[10:11], v[30:31], v[8:9] op_sel_hi:[0,1,1]
	v_pk_fma_f32 v[2:3], v[10:11], v[48:49], v[2:3] op_sel_hi:[0,1,1]
	v_pk_fma_f32 v[4:5], v[10:11], v[32:33], v[4:5] op_sel_hi:[0,1,1]
	v_mul_f32_e32 v10, 0x38800000, v13
	v_mul_f32_e32 v11, v16, v11
	v_div_fixup_f32 v12, v14, v12, 1.0
	v_pk_fma_f32 v[6:7], v[10:11], v[50:51], v[6:7] op_sel_hi:[0,1,1]
	v_pk_fma_f32 v[8:9], v[10:11], v[34:35], v[8:9] op_sel_hi:[0,1,1]
	v_pk_fma_f32 v[2:3], v[10:11], v[52:53], v[2:3] op_sel_hi:[0,1,1]
	v_pk_fma_f32 v[4:5], v[10:11], v[36:37], v[4:5] op_sel_hi:[0,1,1]
	v_mul_f32_e32 v10, 0x38800000, v11
	v_mul_f32_e32 v11, v17, v12
	v_pk_fma_f32 v[6:7], v[10:11], v[54:55], v[6:7] op_sel_hi:[0,1,1]
	v_pk_fma_f32 v[8:9], v[10:11], v[38:39], v[8:9] op_sel_hi:[0,1,1]
	v_pk_fma_f32 v[2:3], v[10:11], v[56:57], v[2:3] op_sel_hi:[0,1,1]
	v_pk_fma_f32 v[4:5], v[10:11], v[40:41], v[4:5] op_sel_hi:[0,1,1]
	v_mul_f32_e32 v10, 0x38800000, v11
	v_pk_fma_f32 v[6:7], v[10:11], v[58:59], v[6:7] op_sel_hi:[0,1,1]
	v_pk_fma_f32 v[8:9], v[10:11], v[42:43], v[8:9] op_sel_hi:[0,1,1]
	v_pk_fma_f32 v[2:3], v[10:11], v[60:61], v[2:3] op_sel_hi:[0,1,1]
	v_pk_fma_f32 v[4:5], v[10:11], v[44:45], v[4:5] op_sel_hi:[0,1,1]
	s_waitcnt vmcnt(23)
	v_max_f32_e32 v46, v94, v94
	v_max_f32_e32 v47, v92, v92
	s_waitcnt vmcnt(22)
	v_max_f32_e32 v50, v90, v90
	v_max_f32_e32 v51, v88, v88
	s_waitcnt vmcnt(21)
	v_max_f32_e32 v54, v86, v86
	v_max_f32_e32 v55, v84, v84
	s_waitcnt vmcnt(20)
	v_max_f32_e32 v58, v82, v82
	v_max_f32_e32 v59, v80, v80
	v_max_f32_e32 v62, v47, v46
	v_max_f32_e32 v63, v51, v50
	v_max_f32_e32 v64, v55, v54
	v_max_f32_e32 v65, v59, v58
	v_sub_f32_e32 v92, v92, v62
	v_sub_f32_e32 v62, v94, v62
	v_mov_b32_e32 v94, v93
	v_sub_f32_e32 v88, v88, v63
	v_sub_f32_e32 v93, v90, v63
	v_mov_b32_e32 v90, v89
	v_sub_f32_e32 v84, v84, v64
	v_sub_f32_e32 v89, v86, v64
	v_mov_b32_e32 v86, v85
	v_sub_f32_e32 v80, v80, v65
	v_sub_f32_e32 v85, v82, v65
	v_mov_b32_e32 v82, v81
	v_mul_f32_e32 v81, 0x3fb8aa3b, v92
	v_mul_f32_e32 v92, 0x3fb8aa3b, v62
	v_mul_f32_e32 v88, 0x3fb8aa3b, v88
	v_mul_f32_e32 v93, 0x3fb8aa3b, v93
	v_mul_f32_e32 v62, 0x3fb8aa3b, v84
	v_mul_f32_e32 v89, 0x3fb8aa3b, v89
	v_mul_f32_e32 v63, 0x3fb8aa3b, v80
	v_mul_f32_e32 v64, 0x3fb8aa3b, v85
	v_exp_f32_e32 v80, v81
	v_exp_f32_e32 v81, v92
	v_exp_f32_e32 v84, v88
	v_exp_f32_e32 v85, v93
	v_exp_f32_e32 v88, v62
	v_exp_f32_e32 v89, v89
	v_exp_f32_e32 v92, v63
	v_exp_f32_e32 v93, v64
	v_pk_mul_f32 v[94:95], v[94:95], v[80:81]
	v_cndmask_b32_e64 v62, v81, v80, s[4:5]
	v_pk_mul_f32 v[80:81], v[90:91], v[84:85]
	v_cndmask_b32_e64 v90, v85, v84, s[4:5]
	v_pk_mul_f32 v[84:85], v[86:87], v[88:89]
	v_cndmask_b32_e64 v86, v89, v88, s[4:5]
	v_pk_mul_f32 v[82:83], v[82:83], v[92:93]
	v_add_f32_e32 v88, v94, v95
	v_add_f32_e32 v80, v80, v81
	v_add_f32_e32 v82, v82, v83
	v_div_scale_f32 v83, s[6:7], v88, v88, 1.0
	v_add_f32_e32 v81, v84, v85
	v_div_scale_f32 v85, s[6:7], v80, v80, 1.0
	v_rcp_f32_e32 v95, v83
	v_div_scale_f32 v91, s[8:9], v81, v81, 1.0
	v_rcp_f32_e32 v63, v85
	v_cndmask_b32_e64 v87, v93, v92, s[4:5]
	v_div_scale_f32 v93, s[10:11], v82, v82, 1.0
	v_rcp_f32_e32 v64, v91
	v_rcp_f32_e32 v65, v93
	v_fma_f32 v66, -v83, v95, 1.0
	v_div_scale_f32 v84, vcc, 1.0, v88, 1.0
	v_fma_f32 v67, -v85, v63, 1.0
	v_fmac_f32_e32 v95, v66, v95
	v_div_scale_f32 v89, s[6:7], 1.0, v80, 1.0
	v_fma_f32 v68, -v91, v64, 1.0
	v_fmac_f32_e32 v63, v67, v63
	v_mul_f32_e32 v66, v84, v95
	v_div_scale_f32 v92, s[8:9], 1.0, v81, 1.0
	v_fma_f32 v69, -v93, v65, 1.0
	v_fmac_f32_e32 v64, v68, v64
	v_mul_f32_e32 v67, v89, v63
	v_fma_f32 v70, -v83, v66, v84
	v_div_scale_f32 v94, s[10:11], 1.0, v82, 1.0
	v_fmac_f32_e32 v65, v69, v65
	v_mul_f32_e32 v68, v92, v64
	v_fma_f32 v71, -v85, v67, v89
	v_fmac_f32_e32 v66, v70, v95
	v_mul_f32_e32 v69, v94, v65
	v_fma_f32 v72, -v91, v68, v92
	v_fmac_f32_e32 v67, v71, v63
	v_fma_f32 v83, -v83, v66, v84
	s_waitcnt vmcnt(19)
	v_cvt_f32_f16_e32 v46, v96
	v_cvt_f32_f16_sdwa v47, v96 dst_sel:DWORD dst_unused:UNUSED_PAD src0_sel:WORD_1
	v_cvt_f32_f16_e32 v96, v97
	v_cvt_f32_f16_sdwa v97, v97 dst_sel:DWORD dst_unused:UNUSED_PAD src0_sel:WORD_1
	v_cvt_f32_f16_e32 v48, v98
	v_cvt_f32_f16_sdwa v49, v98 dst_sel:DWORD dst_unused:UNUSED_PAD src0_sel:WORD_1
	v_cvt_f32_f16_e32 v98, v99
	v_cvt_f32_f16_sdwa v99, v99 dst_sel:DWORD dst_unused:UNUSED_PAD src0_sel:WORD_1
	v_fma_f32 v73, -v93, v69, v94
	v_fmac_f32_e32 v68, v72, v64
	v_fma_f32 v84, -v85, v67, v89
	v_div_fmas_f32 v83, v83, v95, v66
	s_mov_b64 vcc, s[6:7]
	s_waitcnt vmcnt(18)
	v_cvt_f32_f16_e32 v50, v100
	v_cvt_f32_f16_sdwa v51, v100 dst_sel:DWORD dst_unused:UNUSED_PAD src0_sel:WORD_1
	v_cvt_f32_f16_e32 v100, v101
	v_cvt_f32_f16_sdwa v101, v101 dst_sel:DWORD dst_unused:UNUSED_PAD src0_sel:WORD_1
	v_cvt_f32_f16_e32 v52, v102
	v_cvt_f32_f16_sdwa v53, v102 dst_sel:DWORD dst_unused:UNUSED_PAD src0_sel:WORD_1
	v_cvt_f32_f16_e32 v102, v103
	v_cvt_f32_f16_sdwa v103, v103 dst_sel:DWORD dst_unused:UNUSED_PAD src0_sel:WORD_1
	v_fmac_f32_e32 v69, v73, v65
	v_fma_f32 v85, -v91, v68, v92
	v_div_fixup_f32 v83, v83, v88, 1.0
	v_div_fmas_f32 v84, v84, v63, v67
	s_mov_b64 vcc, s[8:9]
	s_waitcnt vmcnt(17)
	v_cvt_f32_f16_e32 v54, v104
	v_cvt_f32_f16_sdwa v55, v104 dst_sel:DWORD dst_unused:UNUSED_PAD src0_sel:WORD_1
	v_cvt_f32_f16_e32 v104, v105
	v_cvt_f32_f16_sdwa v105, v105 dst_sel:DWORD dst_unused:UNUSED_PAD src0_sel:WORD_1
	v_cvt_f32_f16_e32 v56, v106
	v_cvt_f32_f16_sdwa v57, v106 dst_sel:DWORD dst_unused:UNUSED_PAD src0_sel:WORD_1
	v_cvt_f32_f16_e32 v106, v107
	v_cvt_f32_f16_sdwa v107, v107 dst_sel:DWORD dst_unused:UNUSED_PAD src0_sel:WORD_1
	v_fma_f32 v89, -v93, v69, v94
	v_mul_f32_e32 v83, v62, v83
	v_div_fixup_f32 v84, v84, v80, 1.0
	v_div_fmas_f32 v85, v85, v64, v68
	s_mov_b64 vcc, s[10:11]
	s_waitcnt vmcnt(16)
	v_cvt_f32_f16_e32 v58, v108
	v_cvt_f32_f16_sdwa v59, v108 dst_sel:DWORD dst_unused:UNUSED_PAD src0_sel:WORD_1
	v_cvt_f32_f16_e32 v108, v109
	v_cvt_f32_f16_sdwa v109, v109 dst_sel:DWORD dst_unused:UNUSED_PAD src0_sel:WORD_1
	v_cvt_f32_f16_e32 v60, v110
	v_cvt_f32_f16_sdwa v61, v110 dst_sel:DWORD dst_unused:UNUSED_PAD src0_sel:WORD_1
	v_cvt_f32_f16_e32 v110, v111
	v_cvt_f32_f16_sdwa v111, v111 dst_sel:DWORD dst_unused:UNUSED_PAD src0_sel:WORD_1
	v_mul_f32_e32 v80, 0x38800000, v83
	v_mul_f32_e32 v83, v90, v84
	v_div_fixup_f32 v81, v85, v81, 1.0
	v_div_fmas_f32 v84, v89, v65, v69
	v_pk_fma_f32 v[6:7], v[80:81], v[46:47], v[6:7] op_sel_hi:[0,1,1]
	v_pk_fma_f32 v[8:9], v[80:81], v[96:97], v[8:9] op_sel_hi:[0,1,1]
	v_pk_fma_f32 v[2:3], v[80:81], v[48:49], v[2:3] op_sel_hi:[0,1,1]
	v_pk_fma_f32 v[4:5], v[80:81], v[98:99], v[4:5] op_sel_hi:[0,1,1]
	v_mul_f32_e32 v80, 0x38800000, v83
	v_mul_f32_e32 v81, v86, v81
	v_div_fixup_f32 v82, v84, v82, 1.0
	v_pk_fma_f32 v[6:7], v[80:81], v[50:51], v[6:7] op_sel_hi:[0,1,1]
	v_pk_fma_f32 v[8:9], v[80:81], v[100:101], v[8:9] op_sel_hi:[0,1,1]
	v_pk_fma_f32 v[2:3], v[80:81], v[52:53], v[2:3] op_sel_hi:[0,1,1]
	v_pk_fma_f32 v[4:5], v[80:81], v[102:103], v[4:5] op_sel_hi:[0,1,1]
	v_mul_f32_e32 v80, 0x38800000, v81
	v_mul_f32_e32 v81, v87, v82
	v_pk_fma_f32 v[6:7], v[80:81], v[54:55], v[6:7] op_sel_hi:[0,1,1]
	v_pk_fma_f32 v[8:9], v[80:81], v[104:105], v[8:9] op_sel_hi:[0,1,1]
	v_pk_fma_f32 v[2:3], v[80:81], v[56:57], v[2:3] op_sel_hi:[0,1,1]
	v_pk_fma_f32 v[4:5], v[80:81], v[106:107], v[4:5] op_sel_hi:[0,1,1]
	v_mul_f32_e32 v80, 0x38800000, v81
	v_pk_fma_f32 v[6:7], v[80:81], v[58:59], v[6:7] op_sel_hi:[0,1,1]
	v_pk_fma_f32 v[8:9], v[80:81], v[108:109], v[8:9] op_sel_hi:[0,1,1]
	v_pk_fma_f32 v[2:3], v[80:81], v[60:61], v[2:3] op_sel_hi:[0,1,1]
	v_pk_fma_f32 v[4:5], v[80:81], v[110:111], v[4:5] op_sel_hi:[0,1,1]
	s_waitcnt vmcnt(15)
	v_max_f32_e32 v46, v126, v126
	v_max_f32_e32 v47, v124, v124
	s_waitcnt vmcnt(14)
	v_max_f32_e32 v50, v122, v122
	v_max_f32_e32 v51, v120, v120
	s_waitcnt vmcnt(13)
	v_max_f32_e32 v54, v118, v118
	v_max_f32_e32 v55, v116, v116
	s_waitcnt vmcnt(12)
	v_max_f32_e32 v58, v114, v114
	v_max_f32_e32 v59, v112, v112
	v_max_f32_e32 v62, v47, v46
	v_max_f32_e32 v63, v51, v50
	v_max_f32_e32 v64, v55, v54
	v_max_f32_e32 v65, v59, v58
	v_sub_f32_e32 v124, v124, v62
	v_sub_f32_e32 v62, v126, v62
	v_mov_b32_e32 v126, v125
	v_sub_f32_e32 v120, v120, v63
	v_sub_f32_e32 v125, v122, v63
	v_mov_b32_e32 v122, v121
	v_sub_f32_e32 v116, v116, v64
	v_sub_f32_e32 v121, v118, v64
	v_mov_b32_e32 v118, v117
	v_sub_f32_e32 v112, v112, v65
	v_sub_f32_e32 v117, v114, v65
	v_mov_b32_e32 v114, v113
	v_mul_f32_e32 v113, 0x3fb8aa3b, v124
	v_mul_f32_e32 v124, 0x3fb8aa3b, v62
	v_mul_f32_e32 v120, 0x3fb8aa3b, v120
	v_mul_f32_e32 v125, 0x3fb8aa3b, v125
	v_mul_f32_e32 v62, 0x3fb8aa3b, v116
	v_mul_f32_e32 v121, 0x3fb8aa3b, v121
	v_mul_f32_e32 v63, 0x3fb8aa3b, v112
	v_mul_f32_e32 v64, 0x3fb8aa3b, v117
	v_exp_f32_e32 v112, v113
	v_exp_f32_e32 v113, v124
	v_exp_f32_e32 v116, v120
	v_exp_f32_e32 v117, v125
	v_exp_f32_e32 v120, v62
	v_exp_f32_e32 v121, v121
	v_exp_f32_e32 v124, v63
	v_exp_f32_e32 v125, v64
	v_pk_mul_f32 v[126:127], v[126:127], v[112:113]
	v_cndmask_b32_e64 v62, v113, v112, s[4:5]
	v_pk_mul_f32 v[112:113], v[122:123], v[116:117]
	v_cndmask_b32_e64 v122, v117, v116, s[4:5]
	v_pk_mul_f32 v[116:117], v[118:119], v[120:121]
	v_cndmask_b32_e64 v118, v121, v120, s[4:5]
	v_pk_mul_f32 v[114:115], v[114:115], v[124:125]
	v_add_f32_e32 v120, v126, v127
	v_add_f32_e32 v112, v112, v113
	v_add_f32_e32 v114, v114, v115
	v_div_scale_f32 v115, s[6:7], v120, v120, 1.0
	v_add_f32_e32 v113, v116, v117
	v_div_scale_f32 v117, s[6:7], v112, v112, 1.0
	v_rcp_f32_e32 v127, v115
	v_div_scale_f32 v123, s[8:9], v113, v113, 1.0
	v_rcp_f32_e32 v63, v117
	v_cndmask_b32_e64 v119, v125, v124, s[4:5]
	v_div_scale_f32 v125, s[10:11], v114, v114, 1.0
	v_rcp_f32_e32 v64, v123
	v_rcp_f32_e32 v65, v125
	v_fma_f32 v66, -v115, v127, 1.0
	v_div_scale_f32 v116, vcc, 1.0, v120, 1.0
	v_fma_f32 v67, -v117, v63, 1.0
	v_fmac_f32_e32 v127, v66, v127
	v_div_scale_f32 v121, s[6:7], 1.0, v112, 1.0
	v_fma_f32 v68, -v123, v64, 1.0
	v_fmac_f32_e32 v63, v67, v63
	v_mul_f32_e32 v66, v116, v127
	v_div_scale_f32 v124, s[8:9], 1.0, v113, 1.0
	v_fma_f32 v69, -v125, v65, 1.0
	v_fmac_f32_e32 v64, v68, v64
	v_mul_f32_e32 v67, v121, v63
	v_fma_f32 v70, -v115, v66, v116
	v_div_scale_f32 v126, s[10:11], 1.0, v114, 1.0
	v_fmac_f32_e32 v65, v69, v65
	v_mul_f32_e32 v68, v124, v64
	v_fma_f32 v71, -v117, v67, v121
	v_fmac_f32_e32 v66, v70, v127
	v_mul_f32_e32 v69, v126, v65
	v_fma_f32 v72, -v123, v68, v124
	v_fmac_f32_e32 v67, v71, v63
	v_fma_f32 v115, -v115, v66, v116
	s_waitcnt vmcnt(11)
	v_cvt_f32_f16_e32 v46, v128
	v_cvt_f32_f16_sdwa v47, v128 dst_sel:DWORD dst_unused:UNUSED_PAD src0_sel:WORD_1
	v_cvt_f32_f16_e32 v128, v129
	v_cvt_f32_f16_sdwa v129, v129 dst_sel:DWORD dst_unused:UNUSED_PAD src0_sel:WORD_1
	v_cvt_f32_f16_e32 v48, v130
	v_cvt_f32_f16_sdwa v49, v130 dst_sel:DWORD dst_unused:UNUSED_PAD src0_sel:WORD_1
	v_cvt_f32_f16_e32 v130, v131
	v_cvt_f32_f16_sdwa v131, v131 dst_sel:DWORD dst_unused:UNUSED_PAD src0_sel:WORD_1
	v_fma_f32 v73, -v125, v69, v126
	v_fmac_f32_e32 v68, v72, v64
	v_fma_f32 v116, -v117, v67, v121
	v_div_fmas_f32 v115, v115, v127, v66
	s_mov_b64 vcc, s[6:7]
	s_waitcnt vmcnt(10)
	v_cvt_f32_f16_e32 v50, v132
	v_cvt_f32_f16_sdwa v51, v132 dst_sel:DWORD dst_unused:UNUSED_PAD src0_sel:WORD_1
	v_cvt_f32_f16_e32 v132, v133
	v_cvt_f32_f16_sdwa v133, v133 dst_sel:DWORD dst_unused:UNUSED_PAD src0_sel:WORD_1
	v_cvt_f32_f16_e32 v52, v134
	v_cvt_f32_f16_sdwa v53, v134 dst_sel:DWORD dst_unused:UNUSED_PAD src0_sel:WORD_1
	v_cvt_f32_f16_e32 v134, v135
	v_cvt_f32_f16_sdwa v135, v135 dst_sel:DWORD dst_unused:UNUSED_PAD src0_sel:WORD_1
	v_fmac_f32_e32 v69, v73, v65
	v_fma_f32 v117, -v123, v68, v124
	v_div_fixup_f32 v115, v115, v120, 1.0
	v_div_fmas_f32 v116, v116, v63, v67
	s_mov_b64 vcc, s[8:9]
	s_waitcnt vmcnt(9)
	v_cvt_f32_f16_e32 v54, v136
	v_cvt_f32_f16_sdwa v55, v136 dst_sel:DWORD dst_unused:UNUSED_PAD src0_sel:WORD_1
	v_cvt_f32_f16_e32 v136, v137
	v_cvt_f32_f16_sdwa v137, v137 dst_sel:DWORD dst_unused:UNUSED_PAD src0_sel:WORD_1
	v_cvt_f32_f16_e32 v56, v138
	v_cvt_f32_f16_sdwa v57, v138 dst_sel:DWORD dst_unused:UNUSED_PAD src0_sel:WORD_1
	v_cvt_f32_f16_e32 v138, v139
	v_cvt_f32_f16_sdwa v139, v139 dst_sel:DWORD dst_unused:UNUSED_PAD src0_sel:WORD_1
	v_fma_f32 v121, -v125, v69, v126
	v_mul_f32_e32 v115, v62, v115
	v_div_fixup_f32 v116, v116, v112, 1.0
	v_div_fmas_f32 v117, v117, v64, v68
	s_mov_b64 vcc, s[10:11]
	s_waitcnt vmcnt(8)
	v_cvt_f32_f16_e32 v58, v140
	v_cvt_f32_f16_sdwa v59, v140 dst_sel:DWORD dst_unused:UNUSED_PAD src0_sel:WORD_1
	v_cvt_f32_f16_e32 v140, v141
	v_cvt_f32_f16_sdwa v141, v141 dst_sel:DWORD dst_unused:UNUSED_PAD src0_sel:WORD_1
	v_cvt_f32_f16_e32 v60, v142
	v_cvt_f32_f16_sdwa v61, v142 dst_sel:DWORD dst_unused:UNUSED_PAD src0_sel:WORD_1
	v_cvt_f32_f16_e32 v142, v143
	v_cvt_f32_f16_sdwa v143, v143 dst_sel:DWORD dst_unused:UNUSED_PAD src0_sel:WORD_1
	v_mul_f32_e32 v112, 0x38800000, v115
	v_mul_f32_e32 v115, v122, v116
	v_div_fixup_f32 v113, v117, v113, 1.0
	v_div_fmas_f32 v116, v121, v65, v69
	v_pk_fma_f32 v[6:7], v[112:113], v[46:47], v[6:7] op_sel_hi:[0,1,1]
	v_pk_fma_f32 v[8:9], v[112:113], v[128:129], v[8:9] op_sel_hi:[0,1,1]
	v_pk_fma_f32 v[2:3], v[112:113], v[48:49], v[2:3] op_sel_hi:[0,1,1]
	v_pk_fma_f32 v[4:5], v[112:113], v[130:131], v[4:5] op_sel_hi:[0,1,1]
	v_mul_f32_e32 v112, 0x38800000, v115
	v_mul_f32_e32 v113, v118, v113
	v_div_fixup_f32 v114, v116, v114, 1.0
	v_pk_fma_f32 v[6:7], v[112:113], v[50:51], v[6:7] op_sel_hi:[0,1,1]
	v_pk_fma_f32 v[8:9], v[112:113], v[132:133], v[8:9] op_sel_hi:[0,1,1]
	v_pk_fma_f32 v[2:3], v[112:113], v[52:53], v[2:3] op_sel_hi:[0,1,1]
	v_pk_fma_f32 v[4:5], v[112:113], v[134:135], v[4:5] op_sel_hi:[0,1,1]
	v_mul_f32_e32 v112, 0x38800000, v113
	v_mul_f32_e32 v113, v119, v114
	v_pk_fma_f32 v[6:7], v[112:113], v[54:55], v[6:7] op_sel_hi:[0,1,1]
	v_pk_fma_f32 v[8:9], v[112:113], v[136:137], v[8:9] op_sel_hi:[0,1,1]
	v_pk_fma_f32 v[2:3], v[112:113], v[56:57], v[2:3] op_sel_hi:[0,1,1]
	v_pk_fma_f32 v[4:5], v[112:113], v[138:139], v[4:5] op_sel_hi:[0,1,1]
	v_mul_f32_e32 v112, 0x38800000, v113
	v_pk_fma_f32 v[6:7], v[112:113], v[58:59], v[6:7] op_sel_hi:[0,1,1]
	v_pk_fma_f32 v[8:9], v[112:113], v[140:141], v[8:9] op_sel_hi:[0,1,1]
	v_pk_fma_f32 v[2:3], v[112:113], v[60:61], v[2:3] op_sel_hi:[0,1,1]
	v_pk_fma_f32 v[4:5], v[112:113], v[142:143], v[4:5] op_sel_hi:[0,1,1]
	s_waitcnt vmcnt(7)
	v_max_f32_e32 v46, v158, v158
	v_max_f32_e32 v47, v156, v156
	s_waitcnt vmcnt(6)
	v_max_f32_e32 v50, v154, v154
	v_max_f32_e32 v51, v152, v152
	s_waitcnt vmcnt(5)
	v_max_f32_e32 v54, v150, v150
	v_max_f32_e32 v55, v148, v148
	s_waitcnt vmcnt(4)
	v_max_f32_e32 v58, v146, v146
	v_max_f32_e32 v59, v144, v144
	v_max_f32_e32 v62, v47, v46
	v_max_f32_e32 v63, v51, v50
	v_max_f32_e32 v64, v55, v54
	v_max_f32_e32 v65, v59, v58
	v_sub_f32_e32 v156, v156, v62
	v_sub_f32_e32 v62, v158, v62
	v_mov_b32_e32 v158, v157
	v_sub_f32_e32 v152, v152, v63
	v_sub_f32_e32 v157, v154, v63
	v_mov_b32_e32 v154, v153
	v_sub_f32_e32 v148, v148, v64
	v_sub_f32_e32 v153, v150, v64
	v_mov_b32_e32 v150, v149
	v_sub_f32_e32 v144, v144, v65
	v_sub_f32_e32 v149, v146, v65
	v_mov_b32_e32 v146, v145
	v_mul_f32_e32 v145, 0x3fb8aa3b, v156
	v_mul_f32_e32 v156, 0x3fb8aa3b, v62
	v_mul_f32_e32 v152, 0x3fb8aa3b, v152
	v_mul_f32_e32 v157, 0x3fb8aa3b, v157
	v_mul_f32_e32 v62, 0x3fb8aa3b, v148
	v_mul_f32_e32 v153, 0x3fb8aa3b, v153
	v_mul_f32_e32 v63, 0x3fb8aa3b, v144
	v_mul_f32_e32 v64, 0x3fb8aa3b, v149
	v_exp_f32_e32 v144, v145
	v_exp_f32_e32 v145, v156
	v_exp_f32_e32 v148, v152
	v_exp_f32_e32 v149, v157
	v_exp_f32_e32 v152, v62
	v_exp_f32_e32 v153, v153
	v_exp_f32_e32 v156, v63
	v_exp_f32_e32 v157, v64
	v_pk_mul_f32 v[158:159], v[158:159], v[144:145]
	v_cndmask_b32_e64 v62, v145, v144, s[4:5]
	v_pk_mul_f32 v[144:145], v[154:155], v[148:149]
	v_cndmask_b32_e64 v154, v149, v148, s[4:5]
	v_pk_mul_f32 v[148:149], v[150:151], v[152:153]
	v_cndmask_b32_e64 v150, v153, v152, s[4:5]
	v_pk_mul_f32 v[146:147], v[146:147], v[156:157]
	v_add_f32_e32 v152, v158, v159
	v_add_f32_e32 v144, v144, v145
	v_add_f32_e32 v146, v146, v147
	v_div_scale_f32 v147, s[6:7], v152, v152, 1.0
	v_add_f32_e32 v145, v148, v149
	v_div_scale_f32 v149, s[6:7], v144, v144, 1.0
	v_rcp_f32_e32 v159, v147
	v_div_scale_f32 v155, s[8:9], v145, v145, 1.0
	v_rcp_f32_e32 v63, v149
	v_cndmask_b32_e64 v151, v157, v156, s[4:5]
	v_div_scale_f32 v157, s[10:11], v146, v146, 1.0
	v_rcp_f32_e32 v64, v155
	v_rcp_f32_e32 v65, v157
	v_fma_f32 v66, -v147, v159, 1.0
	v_div_scale_f32 v148, vcc, 1.0, v152, 1.0
	v_fma_f32 v67, -v149, v63, 1.0
	v_fmac_f32_e32 v159, v66, v159
	v_div_scale_f32 v153, s[6:7], 1.0, v144, 1.0
	v_fma_f32 v68, -v155, v64, 1.0
	v_fmac_f32_e32 v63, v67, v63
	v_mul_f32_e32 v66, v148, v159
	v_div_scale_f32 v156, s[8:9], 1.0, v145, 1.0
	v_fma_f32 v69, -v157, v65, 1.0
	v_fmac_f32_e32 v64, v68, v64
	v_mul_f32_e32 v67, v153, v63
	v_fma_f32 v70, -v147, v66, v148
	v_div_scale_f32 v158, s[10:11], 1.0, v146, 1.0
	v_fmac_f32_e32 v65, v69, v65
	v_mul_f32_e32 v68, v156, v64
	v_fma_f32 v71, -v149, v67, v153
	v_fmac_f32_e32 v66, v70, v159
	v_mul_f32_e32 v69, v158, v65
	v_fma_f32 v72, -v155, v68, v156
	v_fmac_f32_e32 v67, v71, v63
	v_fma_f32 v147, -v147, v66, v148
	s_waitcnt vmcnt(3)
	v_cvt_f32_f16_e32 v46, v160
	v_cvt_f32_f16_sdwa v47, v160 dst_sel:DWORD dst_unused:UNUSED_PAD src0_sel:WORD_1
	v_cvt_f32_f16_e32 v160, v161
	v_cvt_f32_f16_sdwa v161, v161 dst_sel:DWORD dst_unused:UNUSED_PAD src0_sel:WORD_1
	v_cvt_f32_f16_e32 v48, v162
	v_cvt_f32_f16_sdwa v49, v162 dst_sel:DWORD dst_unused:UNUSED_PAD src0_sel:WORD_1
	v_cvt_f32_f16_e32 v162, v163
	v_cvt_f32_f16_sdwa v163, v163 dst_sel:DWORD dst_unused:UNUSED_PAD src0_sel:WORD_1
	v_fma_f32 v73, -v157, v69, v158
	v_fmac_f32_e32 v68, v72, v64
	v_fma_f32 v148, -v149, v67, v153
	v_div_fmas_f32 v147, v147, v159, v66
	s_mov_b64 vcc, s[6:7]
	s_waitcnt vmcnt(2)
	v_cvt_f32_f16_e32 v50, v164
	v_cvt_f32_f16_sdwa v51, v164 dst_sel:DWORD dst_unused:UNUSED_PAD src0_sel:WORD_1
	v_cvt_f32_f16_e32 v164, v165
	v_cvt_f32_f16_sdwa v165, v165 dst_sel:DWORD dst_unused:UNUSED_PAD src0_sel:WORD_1
	v_cvt_f32_f16_e32 v52, v166
	v_cvt_f32_f16_sdwa v53, v166 dst_sel:DWORD dst_unused:UNUSED_PAD src0_sel:WORD_1
	v_cvt_f32_f16_e32 v166, v167
	v_cvt_f32_f16_sdwa v167, v167 dst_sel:DWORD dst_unused:UNUSED_PAD src0_sel:WORD_1
	v_fmac_f32_e32 v69, v73, v65
	v_fma_f32 v149, -v155, v68, v156
	v_div_fixup_f32 v147, v147, v152, 1.0
	v_div_fmas_f32 v148, v148, v63, v67
	s_mov_b64 vcc, s[8:9]
	s_waitcnt vmcnt(1)
	v_cvt_f32_f16_e32 v54, v168
	v_cvt_f32_f16_sdwa v55, v168 dst_sel:DWORD dst_unused:UNUSED_PAD src0_sel:WORD_1
	v_cvt_f32_f16_e32 v168, v169
	v_cvt_f32_f16_sdwa v169, v169 dst_sel:DWORD dst_unused:UNUSED_PAD src0_sel:WORD_1
	v_cvt_f32_f16_e32 v56, v170
	v_cvt_f32_f16_sdwa v57, v170 dst_sel:DWORD dst_unused:UNUSED_PAD src0_sel:WORD_1
	v_cvt_f32_f16_e32 v170, v171
	v_cvt_f32_f16_sdwa v171, v171 dst_sel:DWORD dst_unused:UNUSED_PAD src0_sel:WORD_1
	v_fma_f32 v153, -v157, v69, v158
	v_mul_f32_e32 v147, v62, v147
	v_div_fixup_f32 v148, v148, v144, 1.0
	v_div_fmas_f32 v149, v149, v64, v68
	s_mov_b64 vcc, s[10:11]
	s_waitcnt vmcnt(0)
	v_cvt_f32_f16_e32 v58, v172
	v_cvt_f32_f16_sdwa v59, v172 dst_sel:DWORD dst_unused:UNUSED_PAD src0_sel:WORD_1
	v_cvt_f32_f16_e32 v172, v173
	v_cvt_f32_f16_sdwa v173, v173 dst_sel:DWORD dst_unused:UNUSED_PAD src0_sel:WORD_1
	v_cvt_f32_f16_e32 v60, v174
	v_cvt_f32_f16_sdwa v61, v174 dst_sel:DWORD dst_unused:UNUSED_PAD src0_sel:WORD_1
	v_cvt_f32_f16_e32 v174, v175
	v_cvt_f32_f16_sdwa v175, v175 dst_sel:DWORD dst_unused:UNUSED_PAD src0_sel:WORD_1
	v_mul_f32_e32 v144, 0x38800000, v147
	v_mul_f32_e32 v147, v154, v148
	v_div_fixup_f32 v145, v149, v145, 1.0
	v_div_fmas_f32 v148, v153, v65, v69
	v_pk_fma_f32 v[6:7], v[144:145], v[46:47], v[6:7] op_sel_hi:[0,1,1]
	v_pk_fma_f32 v[8:9], v[144:145], v[160:161], v[8:9] op_sel_hi:[0,1,1]
	v_pk_fma_f32 v[2:3], v[144:145], v[48:49], v[2:3] op_sel_hi:[0,1,1]
	v_pk_fma_f32 v[4:5], v[144:145], v[162:163], v[4:5] op_sel_hi:[0,1,1]
	v_mul_f32_e32 v144, 0x38800000, v147
	v_mul_f32_e32 v145, v150, v145
	v_div_fixup_f32 v146, v148, v146, 1.0
	v_pk_fma_f32 v[6:7], v[144:145], v[50:51], v[6:7] op_sel_hi:[0,1,1]
	v_pk_fma_f32 v[8:9], v[144:145], v[164:165], v[8:9] op_sel_hi:[0,1,1]
	v_pk_fma_f32 v[2:3], v[144:145], v[52:53], v[2:3] op_sel_hi:[0,1,1]
	v_pk_fma_f32 v[4:5], v[144:145], v[166:167], v[4:5] op_sel_hi:[0,1,1]
	v_mul_f32_e32 v144, 0x38800000, v145
	v_mul_f32_e32 v145, v151, v146
	v_pk_fma_f32 v[6:7], v[144:145], v[54:55], v[6:7] op_sel_hi:[0,1,1]
	v_pk_fma_f32 v[8:9], v[144:145], v[168:169], v[8:9] op_sel_hi:[0,1,1]
	v_pk_fma_f32 v[2:3], v[144:145], v[56:57], v[2:3] op_sel_hi:[0,1,1]
	v_pk_fma_f32 v[4:5], v[144:145], v[170:171], v[4:5] op_sel_hi:[0,1,1]
	v_mul_f32_e32 v144, 0x38800000, v145
	v_pk_fma_f32 v[6:7], v[144:145], v[58:59], v[6:7] op_sel_hi:[0,1,1]
	v_pk_fma_f32 v[8:9], v[144:145], v[172:173], v[8:9] op_sel_hi:[0,1,1]
	v_pk_fma_f32 v[2:3], v[144:145], v[60:61], v[2:3] op_sel_hi:[0,1,1]
	v_pk_fma_f32 v[4:5], v[144:145], v[174:175], v[4:5] op_sel_hi:[0,1,1]
	v_lshlrev_b32_e32 v10, 5, v1
	v_lshl_or_b32 v10, v198, 11, v10
	ds_write_b128 v10, v[6:9]
	ds_write_b128 v10, v[2:5] offset:16
	v_lshlrev_b32_e32 v8, 2, v0
	s_waitcnt lgkmcnt(0)
	s_barrier
	ds_read2st64_b32 v[2:3], v8 offset1:8
	ds_read2st64_b32 v[4:5], v8 offset0:16 offset1:24
	ds_read2st64_b32 v[6:7], v8 offset0:32 offset1:40
	s_lshl_b64 s[4:5], s[20:21], 11
	s_add_u32 s4, s14, s4
	s_waitcnt lgkmcnt(2)
	v_add_f32_e32 v2, 0, v2
	v_add_f32_e32 v9, v2, v3
	ds_read2st64_b32 v[2:3], v8 offset0:48 offset1:56
	s_waitcnt lgkmcnt(2)
	v_add_f32_e32 v4, v9, v4
	v_add_f32_e32 v4, v4, v5
	s_waitcnt lgkmcnt(1)
	v_add_f32_e32 v4, v4, v6
	v_add_f32_e32 v4, v4, v7
	s_waitcnt lgkmcnt(0)
	v_add_f32_e32 v2, v4, v2
	v_add_f32_e32 v2, v2, v3
	s_addc_u32 s5, s15, s5
	global_atomic_add_f32 v8, v2, s[4:5]
	s_branch .LBB4_2
